# v54 + hand-written PEER v-side row loop (8 rows in flight, ids/acts read four at a time, 32-bit row offsets)
# speedup vs baseline: 1.0126x; 1.0076x over previous
.LBB0_1594:
	s_waitcnt lgkmcnt(0)
	v_readfirstlane_b32 s58, v32
	v_readfirstlane_b32 s59, v33
	v_lshlrev_b32_e32 v100, 4, v145
	v_mov_b32_e32 v102, s17
	v_mov_b32_e32 v34, 0
	v_mov_b32_e32 v35, 0
	v_mov_b32_e32 v36, 0
	v_mov_b32_e32 v37, 0
	v_mov_b32_e32 v38, 0
	v_mov_b32_e32 v39, 0
	v_mov_b32_e32 v40, 0
	v_mov_b32_e32 v41, 0
	v_mov_b32_e32 v42, 0
	v_mov_b32_e32 v43, 0
	v_mov_b32_e32 v44, 0
	v_mov_b32_e32 v45, 0
	v_mov_b32_e32 v46, 0
	v_mov_b32_e32 v47, 0
	v_mov_b32_e32 v50, 0
	v_mov_b32_e32 v51, 0
	v_mov_b32_e32 v52, 0
	v_mov_b32_e32 v53, 0
	v_mov_b32_e32 v54, 0
	v_mov_b32_e32 v55, 0
	v_mov_b32_e32 v56, 0
	v_mov_b32_e32 v57, 0
	v_mov_b32_e32 v58, 0
	v_mov_b32_e32 v59, 0
	v_mov_b32_e32 v60, 0
	v_mov_b32_e32 v61, 0
	v_mov_b32_e32 v62, 0
	v_mov_b32_e32 v63, 0
	v_mov_b32_e32 v64, 0
	v_mov_b32_e32 v65, 0
	v_mov_b32_e32 v66, 0
	v_mov_b32_e32 v67, 0
	v_mov_b32_e32 v68, 0
	v_mov_b32_e32 v69, 0
	v_mov_b32_e32 v70, 0
	v_mov_b32_e32 v71, 0
	v_mov_b32_e32 v72, 0
	v_mov_b32_e32 v73, 0
	v_mov_b32_e32 v74, 0
	v_mov_b32_e32 v75, 0
	v_mov_b32_e32 v76, 0
	v_mov_b32_e32 v77, 0
	v_mov_b32_e32 v78, 0
	v_mov_b32_e32 v79, 0
	v_mov_b32_e32 v80, 0
	v_mov_b32_e32 v81, 0
	v_mov_b32_e32 v82, 0
	v_mov_b32_e32 v83, 0
	v_mov_b32_e32 v84, 0
	v_mov_b32_e32 v85, 0
	v_mov_b32_e32 v86, 0
	v_mov_b32_e32 v87, 0
	v_mov_b32_e32 v88, 0
	v_mov_b32_e32 v89, 0
	v_mov_b32_e32 v90, 0
	v_mov_b32_e32 v91, 0
	v_mov_b32_e32 v92, 0
	v_mov_b32_e32 v93, 0
	v_mov_b32_e32 v94, 0
	v_mov_b32_e32 v95, 0
	v_mov_b32_e32 v96, 0
	v_mov_b32_e32 v97, 0
	v_mov_b32_e32 v98, 0
	v_mov_b32_e32 v99, 0
	ds_read_b128 v[212:215], v102
	ds_read_b128 v[216:219], v102 offset:16
	s_waitcnt lgkmcnt(0)
	v_readfirstlane_b32 s60, v212
	v_readfirstlane_b32 s61, v213
	v_readfirstlane_b32 s62, v214
	v_readfirstlane_b32 s63, v215
	s_lshl_b32 s60, s60, 11
	v_add_u32_e32 v101, s60, v100
	global_load_dwordx4 v[148:151], v101, s[58:59]
	global_load_dwordx4 v[152:155], v101, s[58:59] offset:1024
	s_lshl_b32 s61, s61, 11
	v_add_u32_e32 v101, s61, v100
	global_load_dwordx4 v[156:159], v101, s[58:59]
	global_load_dwordx4 v[160:163], v101, s[58:59] offset:1024
	s_lshl_b32 s62, s62, 11
	v_add_u32_e32 v101, s62, v100
	global_load_dwordx4 v[164:167], v101, s[58:59]
	global_load_dwordx4 v[168:171], v101, s[58:59] offset:1024
	s_lshl_b32 s63, s63, 11
	v_add_u32_e32 v101, s63, v100
	global_load_dwordx4 v[172:175], v101, s[58:59]
	global_load_dwordx4 v[176:179], v101, s[58:59] offset:1024
	v_readfirstlane_b32 s60, v216
	v_readfirstlane_b32 s61, v217
	v_readfirstlane_b32 s62, v218
	v_readfirstlane_b32 s63, v219
	s_lshl_b32 s60, s60, 11
	v_add_u32_e32 v101, s60, v100
	global_load_dwordx4 v[180:183], v101, s[58:59]
	global_load_dwordx4 v[184:187], v101, s[58:59] offset:1024
	s_lshl_b32 s61, s61, 11
	v_add_u32_e32 v101, s61, v100
	global_load_dwordx4 v[188:191], v101, s[58:59]
	global_load_dwordx4 v[192:195], v101, s[58:59] offset:1024
	s_lshl_b32 s62, s62, 11
	v_add_u32_e32 v101, s62, v100
	global_load_dwordx4 v[196:199], v101, s[58:59]
	global_load_dwordx4 v[200:203], v101, s[58:59] offset:1024
	s_lshl_b32 s63, s63, 11
	v_add_u32_e32 v101, s63, v100
	global_load_dwordx4 v[204:207], v101, s[58:59]
	global_load_dwordx4 v[208:211], v101, s[58:59] offset:1024
	s_mov_b32 s10, 0
.Lpv_loop:
	ds_read_b128 v[212:215], v102 offset:32
	ds_read_b128 v[216:219], v102 offset:512
	s_waitcnt lgkmcnt(0)
	s_waitcnt vmcnt(14)
	v_cvt_scalef32_pk_f32_fp4 v[220:221], v148, 1.0
	v_pk_fma_f32 v[96:97], v[220:221], v[216:217], v[96:97] op_sel_hi:[1,0,1]
	v_cvt_scalef32_pk_f32_fp4 v[222:223], v148, 1.0 op_sel:[1,0,0]
	v_pk_fma_f32 v[98:99], v[222:223], v[216:217], v[98:99] op_sel_hi:[1,0,1]
	v_cvt_scalef32_pk_f32_fp4 v[224:225], v148, 1.0 op_sel:[0,1,0]
	v_pk_fma_f32 v[94:95], v[224:225], v[216:217], v[94:95] op_sel_hi:[1,0,1]
	v_cvt_scalef32_pk_f32_fp4 v[226:227], v148, 1.0 op_sel:[1,1,0]
	v_pk_fma_f32 v[92:93], v[226:227], v[216:217], v[92:93] op_sel_hi:[1,0,1]
	v_cvt_scalef32_pk_f32_fp4 v[220:221], v149, 1.0
	v_pk_fma_f32 v[90:91], v[220:221], v[216:217], v[90:91] op_sel_hi:[1,0,1]
	v_cvt_scalef32_pk_f32_fp4 v[222:223], v149, 1.0 op_sel:[1,0,0]
	v_pk_fma_f32 v[88:89], v[222:223], v[216:217], v[88:89] op_sel_hi:[1,0,1]
	v_cvt_scalef32_pk_f32_fp4 v[224:225], v149, 1.0 op_sel:[0,1,0]
	v_pk_fma_f32 v[86:87], v[224:225], v[216:217], v[86:87] op_sel_hi:[1,0,1]
	v_cvt_scalef32_pk_f32_fp4 v[226:227], v149, 1.0 op_sel:[1,1,0]
	v_pk_fma_f32 v[84:85], v[226:227], v[216:217], v[84:85] op_sel_hi:[1,0,1]
	v_cvt_scalef32_pk_f32_fp4 v[220:221], v150, 1.0
	v_pk_fma_f32 v[82:83], v[220:221], v[216:217], v[82:83] op_sel_hi:[1,0,1]
	v_cvt_scalef32_pk_f32_fp4 v[222:223], v150, 1.0 op_sel:[1,0,0]
	v_pk_fma_f32 v[80:81], v[222:223], v[216:217], v[80:81] op_sel_hi:[1,0,1]
	v_cvt_scalef32_pk_f32_fp4 v[224:225], v150, 1.0 op_sel:[0,1,0]
	v_pk_fma_f32 v[78:79], v[224:225], v[216:217], v[78:79] op_sel_hi:[1,0,1]
	v_cvt_scalef32_pk_f32_fp4 v[226:227], v150, 1.0 op_sel:[1,1,0]
	v_pk_fma_f32 v[76:77], v[226:227], v[216:217], v[76:77] op_sel_hi:[1,0,1]
	v_cvt_scalef32_pk_f32_fp4 v[220:221], v151, 1.0
	v_pk_fma_f32 v[74:75], v[220:221], v[216:217], v[74:75] op_sel_hi:[1,0,1]
	v_cvt_scalef32_pk_f32_fp4 v[222:223], v151, 1.0 op_sel:[1,0,0]
	v_pk_fma_f32 v[72:73], v[222:223], v[216:217], v[72:73] op_sel_hi:[1,0,1]
	v_cvt_scalef32_pk_f32_fp4 v[224:225], v151, 1.0 op_sel:[0,1,0]
	v_pk_fma_f32 v[70:71], v[224:225], v[216:217], v[70:71] op_sel_hi:[1,0,1]
	v_cvt_scalef32_pk_f32_fp4 v[226:227], v151, 1.0 op_sel:[1,1,0]
	v_pk_fma_f32 v[68:69], v[226:227], v[216:217], v[68:69] op_sel_hi:[1,0,1]
	v_cvt_scalef32_pk_f32_fp4 v[220:221], v152, 1.0
	v_pk_fma_f32 v[66:67], v[220:221], v[216:217], v[66:67] op_sel_hi:[1,0,1]
	v_cvt_scalef32_pk_f32_fp4 v[222:223], v152, 1.0 op_sel:[1,0,0]
	v_pk_fma_f32 v[64:65], v[222:223], v[216:217], v[64:65] op_sel_hi:[1,0,1]
	v_cvt_scalef32_pk_f32_fp4 v[224:225], v152, 1.0 op_sel:[0,1,0]
	v_pk_fma_f32 v[62:63], v[224:225], v[216:217], v[62:63] op_sel_hi:[1,0,1]
	v_cvt_scalef32_pk_f32_fp4 v[226:227], v152, 1.0 op_sel:[1,1,0]
	v_pk_fma_f32 v[60:61], v[226:227], v[216:217], v[60:61] op_sel_hi:[1,0,1]
	v_cvt_scalef32_pk_f32_fp4 v[220:221], v153, 1.0
	v_pk_fma_f32 v[58:59], v[220:221], v[216:217], v[58:59] op_sel_hi:[1,0,1]
	v_cvt_scalef32_pk_f32_fp4 v[222:223], v153, 1.0 op_sel:[1,0,0]
	v_pk_fma_f32 v[56:57], v[222:223], v[216:217], v[56:57] op_sel_hi:[1,0,1]
	v_cvt_scalef32_pk_f32_fp4 v[224:225], v153, 1.0 op_sel:[0,1,0]
	v_pk_fma_f32 v[54:55], v[224:225], v[216:217], v[54:55] op_sel_hi:[1,0,1]
	v_cvt_scalef32_pk_f32_fp4 v[226:227], v153, 1.0 op_sel:[1,1,0]
	v_pk_fma_f32 v[52:53], v[226:227], v[216:217], v[52:53] op_sel_hi:[1,0,1]
	v_cvt_scalef32_pk_f32_fp4 v[220:221], v154, 1.0
	v_pk_fma_f32 v[50:51], v[220:221], v[216:217], v[50:51] op_sel_hi:[1,0,1]
	v_cvt_scalef32_pk_f32_fp4 v[222:223], v154, 1.0 op_sel:[1,0,0]
	v_pk_fma_f32 v[46:47], v[222:223], v[216:217], v[46:47] op_sel_hi:[1,0,1]
	v_cvt_scalef32_pk_f32_fp4 v[224:225], v154, 1.0 op_sel:[0,1,0]
	v_pk_fma_f32 v[44:45], v[224:225], v[216:217], v[44:45] op_sel_hi:[1,0,1]
	v_cvt_scalef32_pk_f32_fp4 v[226:227], v154, 1.0 op_sel:[1,1,0]
	v_pk_fma_f32 v[42:43], v[226:227], v[216:217], v[42:43] op_sel_hi:[1,0,1]
	v_cvt_scalef32_pk_f32_fp4 v[220:221], v155, 1.0
	v_pk_fma_f32 v[40:41], v[220:221], v[216:217], v[40:41] op_sel_hi:[1,0,1]
	v_cvt_scalef32_pk_f32_fp4 v[222:223], v155, 1.0 op_sel:[1,0,0]
	v_pk_fma_f32 v[38:39], v[222:223], v[216:217], v[38:39] op_sel_hi:[1,0,1]
	v_cvt_scalef32_pk_f32_fp4 v[224:225], v155, 1.0 op_sel:[0,1,0]
	v_pk_fma_f32 v[36:37], v[224:225], v[216:217], v[36:37] op_sel_hi:[1,0,1]
	v_cvt_scalef32_pk_f32_fp4 v[226:227], v155, 1.0 op_sel:[1,1,0]
	v_pk_fma_f32 v[34:35], v[226:227], v[216:217], v[34:35] op_sel_hi:[1,0,1]
	s_waitcnt vmcnt(12)
	v_cvt_scalef32_pk_f32_fp4 v[220:221], v156, 1.0
	v_pk_fma_f32 v[96:97], v[220:221], v[216:217], v[96:97] op_sel:[0,1,0] op_sel_hi:[1,1,1]
	v_cvt_scalef32_pk_f32_fp4 v[222:223], v156, 1.0 op_sel:[1,0,0]
	v_pk_fma_f32 v[98:99], v[222:223], v[216:217], v[98:99] op_sel:[0,1,0] op_sel_hi:[1,1,1]
	v_cvt_scalef32_pk_f32_fp4 v[224:225], v156, 1.0 op_sel:[0,1,0]
	v_pk_fma_f32 v[94:95], v[224:225], v[216:217], v[94:95] op_sel:[0,1,0] op_sel_hi:[1,1,1]
	v_cvt_scalef32_pk_f32_fp4 v[226:227], v156, 1.0 op_sel:[1,1,0]
	v_pk_fma_f32 v[92:93], v[226:227], v[216:217], v[92:93] op_sel:[0,1,0] op_sel_hi:[1,1,1]
	v_cvt_scalef32_pk_f32_fp4 v[220:221], v157, 1.0
	v_pk_fma_f32 v[90:91], v[220:221], v[216:217], v[90:91] op_sel:[0,1,0] op_sel_hi:[1,1,1]
	v_cvt_scalef32_pk_f32_fp4 v[222:223], v157, 1.0 op_sel:[1,0,0]
	v_pk_fma_f32 v[88:89], v[222:223], v[216:217], v[88:89] op_sel:[0,1,0] op_sel_hi:[1,1,1]
	v_cvt_scalef32_pk_f32_fp4 v[224:225], v157, 1.0 op_sel:[0,1,0]
	v_pk_fma_f32 v[86:87], v[224:225], v[216:217], v[86:87] op_sel:[0,1,0] op_sel_hi:[1,1,1]
	v_cvt_scalef32_pk_f32_fp4 v[226:227], v157, 1.0 op_sel:[1,1,0]
	v_pk_fma_f32 v[84:85], v[226:227], v[216:217], v[84:85] op_sel:[0,1,0] op_sel_hi:[1,1,1]
	v_cvt_scalef32_pk_f32_fp4 v[220:221], v158, 1.0
	v_pk_fma_f32 v[82:83], v[220:221], v[216:217], v[82:83] op_sel:[0,1,0] op_sel_hi:[1,1,1]
	v_cvt_scalef32_pk_f32_fp4 v[222:223], v158, 1.0 op_sel:[1,0,0]
	v_pk_fma_f32 v[80:81], v[222:223], v[216:217], v[80:81] op_sel:[0,1,0] op_sel_hi:[1,1,1]
	v_cvt_scalef32_pk_f32_fp4 v[224:225], v158, 1.0 op_sel:[0,1,0]
	v_pk_fma_f32 v[78:79], v[224:225], v[216:217], v[78:79] op_sel:[0,1,0] op_sel_hi:[1,1,1]
	v_cvt_scalef32_pk_f32_fp4 v[226:227], v158, 1.0 op_sel:[1,1,0]
	v_pk_fma_f32 v[76:77], v[226:227], v[216:217], v[76:77] op_sel:[0,1,0] op_sel_hi:[1,1,1]
	v_cvt_scalef32_pk_f32_fp4 v[220:221], v159, 1.0
	v_pk_fma_f32 v[74:75], v[220:221], v[216:217], v[74:75] op_sel:[0,1,0] op_sel_hi:[1,1,1]
	v_cvt_scalef32_pk_f32_fp4 v[222:223], v159, 1.0 op_sel:[1,0,0]
	v_pk_fma_f32 v[72:73], v[222:223], v[216:217], v[72:73] op_sel:[0,1,0] op_sel_hi:[1,1,1]
	v_cvt_scalef32_pk_f32_fp4 v[224:225], v159, 1.0 op_sel:[0,1,0]
	v_pk_fma_f32 v[70:71], v[224:225], v[216:217], v[70:71] op_sel:[0,1,0] op_sel_hi:[1,1,1]
	v_cvt_scalef32_pk_f32_fp4 v[226:227], v159, 1.0 op_sel:[1,1,0]
	v_pk_fma_f32 v[68:69], v[226:227], v[216:217], v[68:69] op_sel:[0,1,0] op_sel_hi:[1,1,1]
	v_cvt_scalef32_pk_f32_fp4 v[220:221], v160, 1.0
	v_pk_fma_f32 v[66:67], v[220:221], v[216:217], v[66:67] op_sel:[0,1,0] op_sel_hi:[1,1,1]
	v_cvt_scalef32_pk_f32_fp4 v[222:223], v160, 1.0 op_sel:[1,0,0]
	v_pk_fma_f32 v[64:65], v[222:223], v[216:217], v[64:65] op_sel:[0,1,0] op_sel_hi:[1,1,1]
	v_cvt_scalef32_pk_f32_fp4 v[224:225], v160, 1.0 op_sel:[0,1,0]
	v_pk_fma_f32 v[62:63], v[224:225], v[216:217], v[62:63] op_sel:[0,1,0] op_sel_hi:[1,1,1]
	v_cvt_scalef32_pk_f32_fp4 v[226:227], v160, 1.0 op_sel:[1,1,0]
	v_pk_fma_f32 v[60:61], v[226:227], v[216:217], v[60:61] op_sel:[0,1,0] op_sel_hi:[1,1,1]
	v_cvt_scalef32_pk_f32_fp4 v[220:221], v161, 1.0
	v_pk_fma_f32 v[58:59], v[220:221], v[216:217], v[58:59] op_sel:[0,1,0] op_sel_hi:[1,1,1]
	v_cvt_scalef32_pk_f32_fp4 v[222:223], v161, 1.0 op_sel:[1,0,0]
	v_pk_fma_f32 v[56:57], v[222:223], v[216:217], v[56:57] op_sel:[0,1,0] op_sel_hi:[1,1,1]
	v_cvt_scalef32_pk_f32_fp4 v[224:225], v161, 1.0 op_sel:[0,1,0]
	v_pk_fma_f32 v[54:55], v[224:225], v[216:217], v[54:55] op_sel:[0,1,0] op_sel_hi:[1,1,1]
	v_cvt_scalef32_pk_f32_fp4 v[226:227], v161, 1.0 op_sel:[1,1,0]
	v_pk_fma_f32 v[52:53], v[226:227], v[216:217], v[52:53] op_sel:[0,1,0] op_sel_hi:[1,1,1]
	v_cvt_scalef32_pk_f32_fp4 v[220:221], v162, 1.0
	v_pk_fma_f32 v[50:51], v[220:221], v[216:217], v[50:51] op_sel:[0,1,0] op_sel_hi:[1,1,1]
	v_cvt_scalef32_pk_f32_fp4 v[222:223], v162, 1.0 op_sel:[1,0,0]
	v_pk_fma_f32 v[46:47], v[222:223], v[216:217], v[46:47] op_sel:[0,1,0] op_sel_hi:[1,1,1]
	v_cvt_scalef32_pk_f32_fp4 v[224:225], v162, 1.0 op_sel:[0,1,0]
	v_pk_fma_f32 v[44:45], v[224:225], v[216:217], v[44:45] op_sel:[0,1,0] op_sel_hi:[1,1,1]
	v_cvt_scalef32_pk_f32_fp4 v[226:227], v162, 1.0 op_sel:[1,1,0]
	v_pk_fma_f32 v[42:43], v[226:227], v[216:217], v[42:43] op_sel:[0,1,0] op_sel_hi:[1,1,1]
	v_cvt_scalef32_pk_f32_fp4 v[220:221], v163, 1.0
	v_pk_fma_f32 v[40:41], v[220:221], v[216:217], v[40:41] op_sel:[0,1,0] op_sel_hi:[1,1,1]
	v_cvt_scalef32_pk_f32_fp4 v[222:223], v163, 1.0 op_sel:[1,0,0]
	v_pk_fma_f32 v[38:39], v[222:223], v[216:217], v[38:39] op_sel:[0,1,0] op_sel_hi:[1,1,1]
	v_cvt_scalef32_pk_f32_fp4 v[224:225], v163, 1.0 op_sel:[0,1,0]
	v_pk_fma_f32 v[36:37], v[224:225], v[216:217], v[36:37] op_sel:[0,1,0] op_sel_hi:[1,1,1]
	v_cvt_scalef32_pk_f32_fp4 v[226:227], v163, 1.0 op_sel:[1,1,0]
	v_pk_fma_f32 v[34:35], v[226:227], v[216:217], v[34:35] op_sel:[0,1,0] op_sel_hi:[1,1,1]
	s_waitcnt vmcnt(10)
	v_cvt_scalef32_pk_f32_fp4 v[220:221], v164, 1.0
	v_pk_fma_f32 v[96:97], v[220:221], v[218:219], v[96:97] op_sel_hi:[1,0,1]
	v_cvt_scalef32_pk_f32_fp4 v[222:223], v164, 1.0 op_sel:[1,0,0]
	v_pk_fma_f32 v[98:99], v[222:223], v[218:219], v[98:99] op_sel_hi:[1,0,1]
	v_cvt_scalef32_pk_f32_fp4 v[224:225], v164, 1.0 op_sel:[0,1,0]
	v_pk_fma_f32 v[94:95], v[224:225], v[218:219], v[94:95] op_sel_hi:[1,0,1]
	v_cvt_scalef32_pk_f32_fp4 v[226:227], v164, 1.0 op_sel:[1,1,0]
	v_pk_fma_f32 v[92:93], v[226:227], v[218:219], v[92:93] op_sel_hi:[1,0,1]
	v_cvt_scalef32_pk_f32_fp4 v[220:221], v165, 1.0
	v_pk_fma_f32 v[90:91], v[220:221], v[218:219], v[90:91] op_sel_hi:[1,0,1]
	v_cvt_scalef32_pk_f32_fp4 v[222:223], v165, 1.0 op_sel:[1,0,0]
	v_pk_fma_f32 v[88:89], v[222:223], v[218:219], v[88:89] op_sel_hi:[1,0,1]
	v_cvt_scalef32_pk_f32_fp4 v[224:225], v165, 1.0 op_sel:[0,1,0]
	v_pk_fma_f32 v[86:87], v[224:225], v[218:219], v[86:87] op_sel_hi:[1,0,1]
	v_cvt_scalef32_pk_f32_fp4 v[226:227], v165, 1.0 op_sel:[1,1,0]
	v_pk_fma_f32 v[84:85], v[226:227], v[218:219], v[84:85] op_sel_hi:[1,0,1]
	v_cvt_scalef32_pk_f32_fp4 v[220:221], v166, 1.0
	v_pk_fma_f32 v[82:83], v[220:221], v[218:219], v[82:83] op_sel_hi:[1,0,1]
	v_cvt_scalef32_pk_f32_fp4 v[222:223], v166, 1.0 op_sel:[1,0,0]
	v_pk_fma_f32 v[80:81], v[222:223], v[218:219], v[80:81] op_sel_hi:[1,0,1]
	v_cvt_scalef32_pk_f32_fp4 v[224:225], v166, 1.0 op_sel:[0,1,0]
	v_pk_fma_f32 v[78:79], v[224:225], v[218:219], v[78:79] op_sel_hi:[1,0,1]
	v_cvt_scalef32_pk_f32_fp4 v[226:227], v166, 1.0 op_sel:[1,1,0]
	v_pk_fma_f32 v[76:77], v[226:227], v[218:219], v[76:77] op_sel_hi:[1,0,1]
	v_cvt_scalef32_pk_f32_fp4 v[220:221], v167, 1.0
	v_pk_fma_f32 v[74:75], v[220:221], v[218:219], v[74:75] op_sel_hi:[1,0,1]
	v_cvt_scalef32_pk_f32_fp4 v[222:223], v167, 1.0 op_sel:[1,0,0]
	v_pk_fma_f32 v[72:73], v[222:223], v[218:219], v[72:73] op_sel_hi:[1,0,1]
	v_cvt_scalef32_pk_f32_fp4 v[224:225], v167, 1.0 op_sel:[0,1,0]
	v_pk_fma_f32 v[70:71], v[224:225], v[218:219], v[70:71] op_sel_hi:[1,0,1]
	v_cvt_scalef32_pk_f32_fp4 v[226:227], v167, 1.0 op_sel:[1,1,0]
	v_pk_fma_f32 v[68:69], v[226:227], v[218:219], v[68:69] op_sel_hi:[1,0,1]
	v_cvt_scalef32_pk_f32_fp4 v[220:221], v168, 1.0
	v_pk_fma_f32 v[66:67], v[220:221], v[218:219], v[66:67] op_sel_hi:[1,0,1]
	v_cvt_scalef32_pk_f32_fp4 v[222:223], v168, 1.0 op_sel:[1,0,0]
	v_pk_fma_f32 v[64:65], v[222:223], v[218:219], v[64:65] op_sel_hi:[1,0,1]
	v_cvt_scalef32_pk_f32_fp4 v[224:225], v168, 1.0 op_sel:[0,1,0]
	v_pk_fma_f32 v[62:63], v[224:225], v[218:219], v[62:63] op_sel_hi:[1,0,1]
	v_cvt_scalef32_pk_f32_fp4 v[226:227], v168, 1.0 op_sel:[1,1,0]
	v_pk_fma_f32 v[60:61], v[226:227], v[218:219], v[60:61] op_sel_hi:[1,0,1]
	v_cvt_scalef32_pk_f32_fp4 v[220:221], v169, 1.0
	v_pk_fma_f32 v[58:59], v[220:221], v[218:219], v[58:59] op_sel_hi:[1,0,1]
	v_cvt_scalef32_pk_f32_fp4 v[222:223], v169, 1.0 op_sel:[1,0,0]
	v_pk_fma_f32 v[56:57], v[222:223], v[218:219], v[56:57] op_sel_hi:[1,0,1]
	v_cvt_scalef32_pk_f32_fp4 v[224:225], v169, 1.0 op_sel:[0,1,0]
	v_pk_fma_f32 v[54:55], v[224:225], v[218:219], v[54:55] op_sel_hi:[1,0,1]
	v_cvt_scalef32_pk_f32_fp4 v[226:227], v169, 1.0 op_sel:[1,1,0]
	v_pk_fma_f32 v[52:53], v[226:227], v[218:219], v[52:53] op_sel_hi:[1,0,1]
	v_cvt_scalef32_pk_f32_fp4 v[220:221], v170, 1.0
	v_pk_fma_f32 v[50:51], v[220:221], v[218:219], v[50:51] op_sel_hi:[1,0,1]
	v_cvt_scalef32_pk_f32_fp4 v[222:223], v170, 1.0 op_sel:[1,0,0]
	v_pk_fma_f32 v[46:47], v[222:223], v[218:219], v[46:47] op_sel_hi:[1,0,1]
	v_cvt_scalef32_pk_f32_fp4 v[224:225], v170, 1.0 op_sel:[0,1,0]
	v_pk_fma_f32 v[44:45], v[224:225], v[218:219], v[44:45] op_sel_hi:[1,0,1]
	v_cvt_scalef32_pk_f32_fp4 v[226:227], v170, 1.0 op_sel:[1,1,0]
	v_pk_fma_f32 v[42:43], v[226:227], v[218:219], v[42:43] op_sel_hi:[1,0,1]
	v_cvt_scalef32_pk_f32_fp4 v[220:221], v171, 1.0
	v_pk_fma_f32 v[40:41], v[220:221], v[218:219], v[40:41] op_sel_hi:[1,0,1]
	v_cvt_scalef32_pk_f32_fp4 v[222:223], v171, 1.0 op_sel:[1,0,0]
	v_pk_fma_f32 v[38:39], v[222:223], v[218:219], v[38:39] op_sel_hi:[1,0,1]
	v_cvt_scalef32_pk_f32_fp4 v[224:225], v171, 1.0 op_sel:[0,1,0]
	v_pk_fma_f32 v[36:37], v[224:225], v[218:219], v[36:37] op_sel_hi:[1,0,1]
	v_cvt_scalef32_pk_f32_fp4 v[226:227], v171, 1.0 op_sel:[1,1,0]
	v_pk_fma_f32 v[34:35], v[226:227], v[218:219], v[34:35] op_sel_hi:[1,0,1]
	s_waitcnt vmcnt(8)
	v_cvt_scalef32_pk_f32_fp4 v[220:221], v172, 1.0
	v_pk_fma_f32 v[96:97], v[220:221], v[218:219], v[96:97] op_sel:[0,1,0] op_sel_hi:[1,1,1]
	v_cvt_scalef32_pk_f32_fp4 v[222:223], v172, 1.0 op_sel:[1,0,0]
	v_pk_fma_f32 v[98:99], v[222:223], v[218:219], v[98:99] op_sel:[0,1,0] op_sel_hi:[1,1,1]
	v_cvt_scalef32_pk_f32_fp4 v[224:225], v172, 1.0 op_sel:[0,1,0]
	v_pk_fma_f32 v[94:95], v[224:225], v[218:219], v[94:95] op_sel:[0,1,0] op_sel_hi:[1,1,1]
	v_cvt_scalef32_pk_f32_fp4 v[226:227], v172, 1.0 op_sel:[1,1,0]
	v_pk_fma_f32 v[92:93], v[226:227], v[218:219], v[92:93] op_sel:[0,1,0] op_sel_hi:[1,1,1]
	v_cvt_scalef32_pk_f32_fp4 v[220:221], v173, 1.0
	v_pk_fma_f32 v[90:91], v[220:221], v[218:219], v[90:91] op_sel:[0,1,0] op_sel_hi:[1,1,1]
	v_cvt_scalef32_pk_f32_fp4 v[222:223], v173, 1.0 op_sel:[1,0,0]
	v_pk_fma_f32 v[88:89], v[222:223], v[218:219], v[88:89] op_sel:[0,1,0] op_sel_hi:[1,1,1]
	v_cvt_scalef32_pk_f32_fp4 v[224:225], v173, 1.0 op_sel:[0,1,0]
	v_pk_fma_f32 v[86:87], v[224:225], v[218:219], v[86:87] op_sel:[0,1,0] op_sel_hi:[1,1,1]
	v_cvt_scalef32_pk_f32_fp4 v[226:227], v173, 1.0 op_sel:[1,1,0]
	v_pk_fma_f32 v[84:85], v[226:227], v[218:219], v[84:85] op_sel:[0,1,0] op_sel_hi:[1,1,1]
	v_cvt_scalef32_pk_f32_fp4 v[220:221], v174, 1.0
	v_pk_fma_f32 v[82:83], v[220:221], v[218:219], v[82:83] op_sel:[0,1,0] op_sel_hi:[1,1,1]
	v_cvt_scalef32_pk_f32_fp4 v[222:223], v174, 1.0 op_sel:[1,0,0]
	v_pk_fma_f32 v[80:81], v[222:223], v[218:219], v[80:81] op_sel:[0,1,0] op_sel_hi:[1,1,1]
	v_cvt_scalef32_pk_f32_fp4 v[224:225], v174, 1.0 op_sel:[0,1,0]
	v_pk_fma_f32 v[78:79], v[224:225], v[218:219], v[78:79] op_sel:[0,1,0] op_sel_hi:[1,1,1]
	v_cvt_scalef32_pk_f32_fp4 v[226:227], v174, 1.0 op_sel:[1,1,0]
	v_pk_fma_f32 v[76:77], v[226:227], v[218:219], v[76:77] op_sel:[0,1,0] op_sel_hi:[1,1,1]
	v_cvt_scalef32_pk_f32_fp4 v[220:221], v175, 1.0
	v_pk_fma_f32 v[74:75], v[220:221], v[218:219], v[74:75] op_sel:[0,1,0] op_sel_hi:[1,1,1]
	v_cvt_scalef32_pk_f32_fp4 v[222:223], v175, 1.0 op_sel:[1,0,0]
	v_pk_fma_f32 v[72:73], v[222:223], v[218:219], v[72:73] op_sel:[0,1,0] op_sel_hi:[1,1,1]
	v_cvt_scalef32_pk_f32_fp4 v[224:225], v175, 1.0 op_sel:[0,1,0]
	v_pk_fma_f32 v[70:71], v[224:225], v[218:219], v[70:71] op_sel:[0,1,0] op_sel_hi:[1,1,1]
	v_cvt_scalef32_pk_f32_fp4 v[226:227], v175, 1.0 op_sel:[1,1,0]
	v_pk_fma_f32 v[68:69], v[226:227], v[218:219], v[68:69] op_sel:[0,1,0] op_sel_hi:[1,1,1]
	v_cvt_scalef32_pk_f32_fp4 v[220:221], v176, 1.0
	v_pk_fma_f32 v[66:67], v[220:221], v[218:219], v[66:67] op_sel:[0,1,0] op_sel_hi:[1,1,1]
	v_cvt_scalef32_pk_f32_fp4 v[222:223], v176, 1.0 op_sel:[1,0,0]
	v_pk_fma_f32 v[64:65], v[222:223], v[218:219], v[64:65] op_sel:[0,1,0] op_sel_hi:[1,1,1]
	v_cvt_scalef32_pk_f32_fp4 v[224:225], v176, 1.0 op_sel:[0,1,0]
	v_pk_fma_f32 v[62:63], v[224:225], v[218:219], v[62:63] op_sel:[0,1,0] op_sel_hi:[1,1,1]
	v_cvt_scalef32_pk_f32_fp4 v[226:227], v176, 1.0 op_sel:[1,1,0]
	v_pk_fma_f32 v[60:61], v[226:227], v[218:219], v[60:61] op_sel:[0,1,0] op_sel_hi:[1,1,1]
	v_cvt_scalef32_pk_f32_fp4 v[220:221], v177, 1.0
	v_pk_fma_f32 v[58:59], v[220:221], v[218:219], v[58:59] op_sel:[0,1,0] op_sel_hi:[1,1,1]
	v_cvt_scalef32_pk_f32_fp4 v[222:223], v177, 1.0 op_sel:[1,0,0]
	v_pk_fma_f32 v[56:57], v[222:223], v[218:219], v[56:57] op_sel:[0,1,0] op_sel_hi:[1,1,1]
	v_cvt_scalef32_pk_f32_fp4 v[224:225], v177, 1.0 op_sel:[0,1,0]
	v_pk_fma_f32 v[54:55], v[224:225], v[218:219], v[54:55] op_sel:[0,1,0] op_sel_hi:[1,1,1]
	v_cvt_scalef32_pk_f32_fp4 v[226:227], v177, 1.0 op_sel:[1,1,0]
	v_pk_fma_f32 v[52:53], v[226:227], v[218:219], v[52:53] op_sel:[0,1,0] op_sel_hi:[1,1,1]
	v_cvt_scalef32_pk_f32_fp4 v[220:221], v178, 1.0
	v_pk_fma_f32 v[50:51], v[220:221], v[218:219], v[50:51] op_sel:[0,1,0] op_sel_hi:[1,1,1]
	v_cvt_scalef32_pk_f32_fp4 v[222:223], v178, 1.0 op_sel:[1,0,0]
	v_pk_fma_f32 v[46:47], v[222:223], v[218:219], v[46:47] op_sel:[0,1,0] op_sel_hi:[1,1,1]
	v_cvt_scalef32_pk_f32_fp4 v[224:225], v178, 1.0 op_sel:[0,1,0]
	v_pk_fma_f32 v[44:45], v[224:225], v[218:219], v[44:45] op_sel:[0,1,0] op_sel_hi:[1,1,1]
	v_cvt_scalef32_pk_f32_fp4 v[226:227], v178, 1.0 op_sel:[1,1,0]
	v_pk_fma_f32 v[42:43], v[226:227], v[218:219], v[42:43] op_sel:[0,1,0] op_sel_hi:[1,1,1]
	v_cvt_scalef32_pk_f32_fp4 v[220:221], v179, 1.0
	v_pk_fma_f32 v[40:41], v[220:221], v[218:219], v[40:41] op_sel:[0,1,0] op_sel_hi:[1,1,1]
	v_cvt_scalef32_pk_f32_fp4 v[222:223], v179, 1.0 op_sel:[1,0,0]
	v_pk_fma_f32 v[38:39], v[222:223], v[218:219], v[38:39] op_sel:[0,1,0] op_sel_hi:[1,1,1]
	v_cvt_scalef32_pk_f32_fp4 v[224:225], v179, 1.0 op_sel:[0,1,0]
	v_pk_fma_f32 v[36:37], v[224:225], v[218:219], v[36:37] op_sel:[0,1,0] op_sel_hi:[1,1,1]
	v_cvt_scalef32_pk_f32_fp4 v[226:227], v179, 1.0 op_sel:[1,1,0]
	v_pk_fma_f32 v[34:35], v[226:227], v[218:219], v[34:35] op_sel:[0,1,0] op_sel_hi:[1,1,1]
	v_readfirstlane_b32 s60, v212
	v_readfirstlane_b32 s61, v213
	v_readfirstlane_b32 s62, v214
	v_readfirstlane_b32 s63, v215
	s_lshl_b32 s60, s60, 11
	v_add_u32_e32 v101, s60, v100
	global_load_dwordx4 v[148:151], v101, s[58:59]
	global_load_dwordx4 v[152:155], v101, s[58:59] offset:1024
	s_lshl_b32 s61, s61, 11
	v_add_u32_e32 v101, s61, v100
	global_load_dwordx4 v[156:159], v101, s[58:59]
	global_load_dwordx4 v[160:163], v101, s[58:59] offset:1024
	s_lshl_b32 s62, s62, 11
	v_add_u32_e32 v101, s62, v100
	global_load_dwordx4 v[164:167], v101, s[58:59]
	global_load_dwordx4 v[168:171], v101, s[58:59] offset:1024
	s_lshl_b32 s63, s63, 11
	v_add_u32_e32 v101, s63, v100
	global_load_dwordx4 v[172:175], v101, s[58:59]
	global_load_dwordx4 v[176:179], v101, s[58:59] offset:1024
	ds_read_b128 v[212:215], v102 offset:48
	ds_read_b128 v[216:219], v102 offset:528
	s_waitcnt lgkmcnt(0)
	s_waitcnt vmcnt(14)
	v_cvt_scalef32_pk_f32_fp4 v[220:221], v180, 1.0
	v_pk_fma_f32 v[96:97], v[220:221], v[216:217], v[96:97] op_sel_hi:[1,0,1]
	v_cvt_scalef32_pk_f32_fp4 v[222:223], v180, 1.0 op_sel:[1,0,0]
	v_pk_fma_f32 v[98:99], v[222:223], v[216:217], v[98:99] op_sel_hi:[1,0,1]
	v_cvt_scalef32_pk_f32_fp4 v[224:225], v180, 1.0 op_sel:[0,1,0]
	v_pk_fma_f32 v[94:95], v[224:225], v[216:217], v[94:95] op_sel_hi:[1,0,1]
	v_cvt_scalef32_pk_f32_fp4 v[226:227], v180, 1.0 op_sel:[1,1,0]
	v_pk_fma_f32 v[92:93], v[226:227], v[216:217], v[92:93] op_sel_hi:[1,0,1]
	v_cvt_scalef32_pk_f32_fp4 v[220:221], v181, 1.0
	v_pk_fma_f32 v[90:91], v[220:221], v[216:217], v[90:91] op_sel_hi:[1,0,1]
	v_cvt_scalef32_pk_f32_fp4 v[222:223], v181, 1.0 op_sel:[1,0,0]
	v_pk_fma_f32 v[88:89], v[222:223], v[216:217], v[88:89] op_sel_hi:[1,0,1]
	v_cvt_scalef32_pk_f32_fp4 v[224:225], v181, 1.0 op_sel:[0,1,0]
	v_pk_fma_f32 v[86:87], v[224:225], v[216:217], v[86:87] op_sel_hi:[1,0,1]
	v_cvt_scalef32_pk_f32_fp4 v[226:227], v181, 1.0 op_sel:[1,1,0]
	v_pk_fma_f32 v[84:85], v[226:227], v[216:217], v[84:85] op_sel_hi:[1,0,1]
	v_cvt_scalef32_pk_f32_fp4 v[220:221], v182, 1.0
	v_pk_fma_f32 v[82:83], v[220:221], v[216:217], v[82:83] op_sel_hi:[1,0,1]
	v_cvt_scalef32_pk_f32_fp4 v[222:223], v182, 1.0 op_sel:[1,0,0]
	v_pk_fma_f32 v[80:81], v[222:223], v[216:217], v[80:81] op_sel_hi:[1,0,1]
	v_cvt_scalef32_pk_f32_fp4 v[224:225], v182, 1.0 op_sel:[0,1,0]
	v_pk_fma_f32 v[78:79], v[224:225], v[216:217], v[78:79] op_sel_hi:[1,0,1]
	v_cvt_scalef32_pk_f32_fp4 v[226:227], v182, 1.0 op_sel:[1,1,0]
	v_pk_fma_f32 v[76:77], v[226:227], v[216:217], v[76:77] op_sel_hi:[1,0,1]
	v_cvt_scalef32_pk_f32_fp4 v[220:221], v183, 1.0
	v_pk_fma_f32 v[74:75], v[220:221], v[216:217], v[74:75] op_sel_hi:[1,0,1]
	v_cvt_scalef32_pk_f32_fp4 v[222:223], v183, 1.0 op_sel:[1,0,0]
	v_pk_fma_f32 v[72:73], v[222:223], v[216:217], v[72:73] op_sel_hi:[1,0,1]
	v_cvt_scalef32_pk_f32_fp4 v[224:225], v183, 1.0 op_sel:[0,1,0]
	v_pk_fma_f32 v[70:71], v[224:225], v[216:217], v[70:71] op_sel_hi:[1,0,1]
	v_cvt_scalef32_pk_f32_fp4 v[226:227], v183, 1.0 op_sel:[1,1,0]
	v_pk_fma_f32 v[68:69], v[226:227], v[216:217], v[68:69] op_sel_hi:[1,0,1]
	v_cvt_scalef32_pk_f32_fp4 v[220:221], v184, 1.0
	v_pk_fma_f32 v[66:67], v[220:221], v[216:217], v[66:67] op_sel_hi:[1,0,1]
	v_cvt_scalef32_pk_f32_fp4 v[222:223], v184, 1.0 op_sel:[1,0,0]
	v_pk_fma_f32 v[64:65], v[222:223], v[216:217], v[64:65] op_sel_hi:[1,0,1]
	v_cvt_scalef32_pk_f32_fp4 v[224:225], v184, 1.0 op_sel:[0,1,0]
	v_pk_fma_f32 v[62:63], v[224:225], v[216:217], v[62:63] op_sel_hi:[1,0,1]
	v_cvt_scalef32_pk_f32_fp4 v[226:227], v184, 1.0 op_sel:[1,1,0]
	v_pk_fma_f32 v[60:61], v[226:227], v[216:217], v[60:61] op_sel_hi:[1,0,1]
	v_cvt_scalef32_pk_f32_fp4 v[220:221], v185, 1.0
	v_pk_fma_f32 v[58:59], v[220:221], v[216:217], v[58:59] op_sel_hi:[1,0,1]
	v_cvt_scalef32_pk_f32_fp4 v[222:223], v185, 1.0 op_sel:[1,0,0]
	v_pk_fma_f32 v[56:57], v[222:223], v[216:217], v[56:57] op_sel_hi:[1,0,1]
	v_cvt_scalef32_pk_f32_fp4 v[224:225], v185, 1.0 op_sel:[0,1,0]
	v_pk_fma_f32 v[54:55], v[224:225], v[216:217], v[54:55] op_sel_hi:[1,0,1]
	v_cvt_scalef32_pk_f32_fp4 v[226:227], v185, 1.0 op_sel:[1,1,0]
	v_pk_fma_f32 v[52:53], v[226:227], v[216:217], v[52:53] op_sel_hi:[1,0,1]
	v_cvt_scalef32_pk_f32_fp4 v[220:221], v186, 1.0
	v_pk_fma_f32 v[50:51], v[220:221], v[216:217], v[50:51] op_sel_hi:[1,0,1]
	v_cvt_scalef32_pk_f32_fp4 v[222:223], v186, 1.0 op_sel:[1,0,0]
	v_pk_fma_f32 v[46:47], v[222:223], v[216:217], v[46:47] op_sel_hi:[1,0,1]
	v_cvt_scalef32_pk_f32_fp4 v[224:225], v186, 1.0 op_sel:[0,1,0]
	v_pk_fma_f32 v[44:45], v[224:225], v[216:217], v[44:45] op_sel_hi:[1,0,1]
	v_cvt_scalef32_pk_f32_fp4 v[226:227], v186, 1.0 op_sel:[1,1,0]
	v_pk_fma_f32 v[42:43], v[226:227], v[216:217], v[42:43] op_sel_hi:[1,0,1]
	v_cvt_scalef32_pk_f32_fp4 v[220:221], v187, 1.0
	v_pk_fma_f32 v[40:41], v[220:221], v[216:217], v[40:41] op_sel_hi:[1,0,1]
	v_cvt_scalef32_pk_f32_fp4 v[222:223], v187, 1.0 op_sel:[1,0,0]
	v_pk_fma_f32 v[38:39], v[222:223], v[216:217], v[38:39] op_sel_hi:[1,0,1]
	v_cvt_scalef32_pk_f32_fp4 v[224:225], v187, 1.0 op_sel:[0,1,0]
	v_pk_fma_f32 v[36:37], v[224:225], v[216:217], v[36:37] op_sel_hi:[1,0,1]
	v_cvt_scalef32_pk_f32_fp4 v[226:227], v187, 1.0 op_sel:[1,1,0]
	v_pk_fma_f32 v[34:35], v[226:227], v[216:217], v[34:35] op_sel_hi:[1,0,1]
	s_waitcnt vmcnt(12)
	v_cvt_scalef32_pk_f32_fp4 v[220:221], v188, 1.0
	v_pk_fma_f32 v[96:97], v[220:221], v[216:217], v[96:97] op_sel:[0,1,0] op_sel_hi:[1,1,1]
	v_cvt_scalef32_pk_f32_fp4 v[222:223], v188, 1.0 op_sel:[1,0,0]
	v_pk_fma_f32 v[98:99], v[222:223], v[216:217], v[98:99] op_sel:[0,1,0] op_sel_hi:[1,1,1]
	v_cvt_scalef32_pk_f32_fp4 v[224:225], v188, 1.0 op_sel:[0,1,0]
	v_pk_fma_f32 v[94:95], v[224:225], v[216:217], v[94:95] op_sel:[0,1,0] op_sel_hi:[1,1,1]
	v_cvt_scalef32_pk_f32_fp4 v[226:227], v188, 1.0 op_sel:[1,1,0]
	v_pk_fma_f32 v[92:93], v[226:227], v[216:217], v[92:93] op_sel:[0,1,0] op_sel_hi:[1,1,1]
	v_cvt_scalef32_pk_f32_fp4 v[220:221], v189, 1.0
	v_pk_fma_f32 v[90:91], v[220:221], v[216:217], v[90:91] op_sel:[0,1,0] op_sel_hi:[1,1,1]
	v_cvt_scalef32_pk_f32_fp4 v[222:223], v189, 1.0 op_sel:[1,0,0]
	v_pk_fma_f32 v[88:89], v[222:223], v[216:217], v[88:89] op_sel:[0,1,0] op_sel_hi:[1,1,1]
	v_cvt_scalef32_pk_f32_fp4 v[224:225], v189, 1.0 op_sel:[0,1,0]
	v_pk_fma_f32 v[86:87], v[224:225], v[216:217], v[86:87] op_sel:[0,1,0] op_sel_hi:[1,1,1]
	v_cvt_scalef32_pk_f32_fp4 v[226:227], v189, 1.0 op_sel:[1,1,0]
	v_pk_fma_f32 v[84:85], v[226:227], v[216:217], v[84:85] op_sel:[0,1,0] op_sel_hi:[1,1,1]
	v_cvt_scalef32_pk_f32_fp4 v[220:221], v190, 1.0
	v_pk_fma_f32 v[82:83], v[220:221], v[216:217], v[82:83] op_sel:[0,1,0] op_sel_hi:[1,1,1]
	v_cvt_scalef32_pk_f32_fp4 v[222:223], v190, 1.0 op_sel:[1,0,0]
	v_pk_fma_f32 v[80:81], v[222:223], v[216:217], v[80:81] op_sel:[0,1,0] op_sel_hi:[1,1,1]
	v_cvt_scalef32_pk_f32_fp4 v[224:225], v190, 1.0 op_sel:[0,1,0]
	v_pk_fma_f32 v[78:79], v[224:225], v[216:217], v[78:79] op_sel:[0,1,0] op_sel_hi:[1,1,1]
	v_cvt_scalef32_pk_f32_fp4 v[226:227], v190, 1.0 op_sel:[1,1,0]
	v_pk_fma_f32 v[76:77], v[226:227], v[216:217], v[76:77] op_sel:[0,1,0] op_sel_hi:[1,1,1]
	v_cvt_scalef32_pk_f32_fp4 v[220:221], v191, 1.0
	v_pk_fma_f32 v[74:75], v[220:221], v[216:217], v[74:75] op_sel:[0,1,0] op_sel_hi:[1,1,1]
	v_cvt_scalef32_pk_f32_fp4 v[222:223], v191, 1.0 op_sel:[1,0,0]
	v_pk_fma_f32 v[72:73], v[222:223], v[216:217], v[72:73] op_sel:[0,1,0] op_sel_hi:[1,1,1]
	v_cvt_scalef32_pk_f32_fp4 v[224:225], v191, 1.0 op_sel:[0,1,0]
	v_pk_fma_f32 v[70:71], v[224:225], v[216:217], v[70:71] op_sel:[0,1,0] op_sel_hi:[1,1,1]
	v_cvt_scalef32_pk_f32_fp4 v[226:227], v191, 1.0 op_sel:[1,1,0]
	v_pk_fma_f32 v[68:69], v[226:227], v[216:217], v[68:69] op_sel:[0,1,0] op_sel_hi:[1,1,1]
	v_cvt_scalef32_pk_f32_fp4 v[220:221], v192, 1.0
	v_pk_fma_f32 v[66:67], v[220:221], v[216:217], v[66:67] op_sel:[0,1,0] op_sel_hi:[1,1,1]
	v_cvt_scalef32_pk_f32_fp4 v[222:223], v192, 1.0 op_sel:[1,0,0]
	v_pk_fma_f32 v[64:65], v[222:223], v[216:217], v[64:65] op_sel:[0,1,0] op_sel_hi:[1,1,1]
	v_cvt_scalef32_pk_f32_fp4 v[224:225], v192, 1.0 op_sel:[0,1,0]
	v_pk_fma_f32 v[62:63], v[224:225], v[216:217], v[62:63] op_sel:[0,1,0] op_sel_hi:[1,1,1]
	v_cvt_scalef32_pk_f32_fp4 v[226:227], v192, 1.0 op_sel:[1,1,0]
	v_pk_fma_f32 v[60:61], v[226:227], v[216:217], v[60:61] op_sel:[0,1,0] op_sel_hi:[1,1,1]
	v_cvt_scalef32_pk_f32_fp4 v[220:221], v193, 1.0
	v_pk_fma_f32 v[58:59], v[220:221], v[216:217], v[58:59] op_sel:[0,1,0] op_sel_hi:[1,1,1]
	v_cvt_scalef32_pk_f32_fp4 v[222:223], v193, 1.0 op_sel:[1,0,0]
	v_pk_fma_f32 v[56:57], v[222:223], v[216:217], v[56:57] op_sel:[0,1,0] op_sel_hi:[1,1,1]
	v_cvt_scalef32_pk_f32_fp4 v[224:225], v193, 1.0 op_sel:[0,1,0]
	v_pk_fma_f32 v[54:55], v[224:225], v[216:217], v[54:55] op_sel:[0,1,0] op_sel_hi:[1,1,1]
	v_cvt_scalef32_pk_f32_fp4 v[226:227], v193, 1.0 op_sel:[1,1,0]
	v_pk_fma_f32 v[52:53], v[226:227], v[216:217], v[52:53] op_sel:[0,1,0] op_sel_hi:[1,1,1]
	v_cvt_scalef32_pk_f32_fp4 v[220:221], v194, 1.0
	v_pk_fma_f32 v[50:51], v[220:221], v[216:217], v[50:51] op_sel:[0,1,0] op_sel_hi:[1,1,1]
	v_cvt_scalef32_pk_f32_fp4 v[222:223], v194, 1.0 op_sel:[1,0,0]
	v_pk_fma_f32 v[46:47], v[222:223], v[216:217], v[46:47] op_sel:[0,1,0] op_sel_hi:[1,1,1]
	v_cvt_scalef32_pk_f32_fp4 v[224:225], v194, 1.0 op_sel:[0,1,0]
	v_pk_fma_f32 v[44:45], v[224:225], v[216:217], v[44:45] op_sel:[0,1,0] op_sel_hi:[1,1,1]
	v_cvt_scalef32_pk_f32_fp4 v[226:227], v194, 1.0 op_sel:[1,1,0]
	v_pk_fma_f32 v[42:43], v[226:227], v[216:217], v[42:43] op_sel:[0,1,0] op_sel_hi:[1,1,1]
	v_cvt_scalef32_pk_f32_fp4 v[220:221], v195, 1.0
	v_pk_fma_f32 v[40:41], v[220:221], v[216:217], v[40:41] op_sel:[0,1,0] op_sel_hi:[1,1,1]
	v_cvt_scalef32_pk_f32_fp4 v[222:223], v195, 1.0 op_sel:[1,0,0]
	v_pk_fma_f32 v[38:39], v[222:223], v[216:217], v[38:39] op_sel:[0,1,0] op_sel_hi:[1,1,1]
	v_cvt_scalef32_pk_f32_fp4 v[224:225], v195, 1.0 op_sel:[0,1,0]
	v_pk_fma_f32 v[36:37], v[224:225], v[216:217], v[36:37] op_sel:[0,1,0] op_sel_hi:[1,1,1]
	v_cvt_scalef32_pk_f32_fp4 v[226:227], v195, 1.0 op_sel:[1,1,0]
	v_pk_fma_f32 v[34:35], v[226:227], v[216:217], v[34:35] op_sel:[0,1,0] op_sel_hi:[1,1,1]
	s_waitcnt vmcnt(10)
	v_cvt_scalef32_pk_f32_fp4 v[220:221], v196, 1.0
	v_pk_fma_f32 v[96:97], v[220:221], v[218:219], v[96:97] op_sel_hi:[1,0,1]
	v_cvt_scalef32_pk_f32_fp4 v[222:223], v196, 1.0 op_sel:[1,0,0]
	v_pk_fma_f32 v[98:99], v[222:223], v[218:219], v[98:99] op_sel_hi:[1,0,1]
	v_cvt_scalef32_pk_f32_fp4 v[224:225], v196, 1.0 op_sel:[0,1,0]
	v_pk_fma_f32 v[94:95], v[224:225], v[218:219], v[94:95] op_sel_hi:[1,0,1]
	v_cvt_scalef32_pk_f32_fp4 v[226:227], v196, 1.0 op_sel:[1,1,0]
	v_pk_fma_f32 v[92:93], v[226:227], v[218:219], v[92:93] op_sel_hi:[1,0,1]
	v_cvt_scalef32_pk_f32_fp4 v[220:221], v197, 1.0
	v_pk_fma_f32 v[90:91], v[220:221], v[218:219], v[90:91] op_sel_hi:[1,0,1]
	v_cvt_scalef32_pk_f32_fp4 v[222:223], v197, 1.0 op_sel:[1,0,0]
	v_pk_fma_f32 v[88:89], v[222:223], v[218:219], v[88:89] op_sel_hi:[1,0,1]
	v_cvt_scalef32_pk_f32_fp4 v[224:225], v197, 1.0 op_sel:[0,1,0]
	v_pk_fma_f32 v[86:87], v[224:225], v[218:219], v[86:87] op_sel_hi:[1,0,1]
	v_cvt_scalef32_pk_f32_fp4 v[226:227], v197, 1.0 op_sel:[1,1,0]
	v_pk_fma_f32 v[84:85], v[226:227], v[218:219], v[84:85] op_sel_hi:[1,0,1]
	v_cvt_scalef32_pk_f32_fp4 v[220:221], v198, 1.0
	v_pk_fma_f32 v[82:83], v[220:221], v[218:219], v[82:83] op_sel_hi:[1,0,1]
	v_cvt_scalef32_pk_f32_fp4 v[222:223], v198, 1.0 op_sel:[1,0,0]
	v_pk_fma_f32 v[80:81], v[222:223], v[218:219], v[80:81] op_sel_hi:[1,0,1]
	v_cvt_scalef32_pk_f32_fp4 v[224:225], v198, 1.0 op_sel:[0,1,0]
	v_pk_fma_f32 v[78:79], v[224:225], v[218:219], v[78:79] op_sel_hi:[1,0,1]
	v_cvt_scalef32_pk_f32_fp4 v[226:227], v198, 1.0 op_sel:[1,1,0]
	v_pk_fma_f32 v[76:77], v[226:227], v[218:219], v[76:77] op_sel_hi:[1,0,1]
	v_cvt_scalef32_pk_f32_fp4 v[220:221], v199, 1.0
	v_pk_fma_f32 v[74:75], v[220:221], v[218:219], v[74:75] op_sel_hi:[1,0,1]
	v_cvt_scalef32_pk_f32_fp4 v[222:223], v199, 1.0 op_sel:[1,0,0]
	v_pk_fma_f32 v[72:73], v[222:223], v[218:219], v[72:73] op_sel_hi:[1,0,1]
	v_cvt_scalef32_pk_f32_fp4 v[224:225], v199, 1.0 op_sel:[0,1,0]
	v_pk_fma_f32 v[70:71], v[224:225], v[218:219], v[70:71] op_sel_hi:[1,0,1]
	v_cvt_scalef32_pk_f32_fp4 v[226:227], v199, 1.0 op_sel:[1,1,0]
	v_pk_fma_f32 v[68:69], v[226:227], v[218:219], v[68:69] op_sel_hi:[1,0,1]
	v_cvt_scalef32_pk_f32_fp4 v[220:221], v200, 1.0
	v_pk_fma_f32 v[66:67], v[220:221], v[218:219], v[66:67] op_sel_hi:[1,0,1]
	v_cvt_scalef32_pk_f32_fp4 v[222:223], v200, 1.0 op_sel:[1,0,0]
	v_pk_fma_f32 v[64:65], v[222:223], v[218:219], v[64:65] op_sel_hi:[1,0,1]
	v_cvt_scalef32_pk_f32_fp4 v[224:225], v200, 1.0 op_sel:[0,1,0]
	v_pk_fma_f32 v[62:63], v[224:225], v[218:219], v[62:63] op_sel_hi:[1,0,1]
	v_cvt_scalef32_pk_f32_fp4 v[226:227], v200, 1.0 op_sel:[1,1,0]
	v_pk_fma_f32 v[60:61], v[226:227], v[218:219], v[60:61] op_sel_hi:[1,0,1]
	v_cvt_scalef32_pk_f32_fp4 v[220:221], v201, 1.0
	v_pk_fma_f32 v[58:59], v[220:221], v[218:219], v[58:59] op_sel_hi:[1,0,1]
	v_cvt_scalef32_pk_f32_fp4 v[222:223], v201, 1.0 op_sel:[1,0,0]
	v_pk_fma_f32 v[56:57], v[222:223], v[218:219], v[56:57] op_sel_hi:[1,0,1]
	v_cvt_scalef32_pk_f32_fp4 v[224:225], v201, 1.0 op_sel:[0,1,0]
	v_pk_fma_f32 v[54:55], v[224:225], v[218:219], v[54:55] op_sel_hi:[1,0,1]
	v_cvt_scalef32_pk_f32_fp4 v[226:227], v201, 1.0 op_sel:[1,1,0]
	v_pk_fma_f32 v[52:53], v[226:227], v[218:219], v[52:53] op_sel_hi:[1,0,1]
	v_cvt_scalef32_pk_f32_fp4 v[220:221], v202, 1.0
	v_pk_fma_f32 v[50:51], v[220:221], v[218:219], v[50:51] op_sel_hi:[1,0,1]
	v_cvt_scalef32_pk_f32_fp4 v[222:223], v202, 1.0 op_sel:[1,0,0]
	v_pk_fma_f32 v[46:47], v[222:223], v[218:219], v[46:47] op_sel_hi:[1,0,1]
	v_cvt_scalef32_pk_f32_fp4 v[224:225], v202, 1.0 op_sel:[0,1,0]
	v_pk_fma_f32 v[44:45], v[224:225], v[218:219], v[44:45] op_sel_hi:[1,0,1]
	v_cvt_scalef32_pk_f32_fp4 v[226:227], v202, 1.0 op_sel:[1,1,0]
	v_pk_fma_f32 v[42:43], v[226:227], v[218:219], v[42:43] op_sel_hi:[1,0,1]
	v_cvt_scalef32_pk_f32_fp4 v[220:221], v203, 1.0
	v_pk_fma_f32 v[40:41], v[220:221], v[218:219], v[40:41] op_sel_hi:[1,0,1]
	v_cvt_scalef32_pk_f32_fp4 v[222:223], v203, 1.0 op_sel:[1,0,0]
	v_pk_fma_f32 v[38:39], v[222:223], v[218:219], v[38:39] op_sel_hi:[1,0,1]
	v_cvt_scalef32_pk_f32_fp4 v[224:225], v203, 1.0 op_sel:[0,1,0]
	v_pk_fma_f32 v[36:37], v[224:225], v[218:219], v[36:37] op_sel_hi:[1,0,1]
	v_cvt_scalef32_pk_f32_fp4 v[226:227], v203, 1.0 op_sel:[1,1,0]
	v_pk_fma_f32 v[34:35], v[226:227], v[218:219], v[34:35] op_sel_hi:[1,0,1]
	s_waitcnt vmcnt(8)
	v_cvt_scalef32_pk_f32_fp4 v[220:221], v204, 1.0
	v_pk_fma_f32 v[96:97], v[220:221], v[218:219], v[96:97] op_sel:[0,1,0] op_sel_hi:[1,1,1]
	v_cvt_scalef32_pk_f32_fp4 v[222:223], v204, 1.0 op_sel:[1,0,0]
	v_pk_fma_f32 v[98:99], v[222:223], v[218:219], v[98:99] op_sel:[0,1,0] op_sel_hi:[1,1,1]
	v_cvt_scalef32_pk_f32_fp4 v[224:225], v204, 1.0 op_sel:[0,1,0]
	v_pk_fma_f32 v[94:95], v[224:225], v[218:219], v[94:95] op_sel:[0,1,0] op_sel_hi:[1,1,1]
	v_cvt_scalef32_pk_f32_fp4 v[226:227], v204, 1.0 op_sel:[1,1,0]
	v_pk_fma_f32 v[92:93], v[226:227], v[218:219], v[92:93] op_sel:[0,1,0] op_sel_hi:[1,1,1]
	v_cvt_scalef32_pk_f32_fp4 v[220:221], v205, 1.0
	v_pk_fma_f32 v[90:91], v[220:221], v[218:219], v[90:91] op_sel:[0,1,0] op_sel_hi:[1,1,1]
	v_cvt_scalef32_pk_f32_fp4 v[222:223], v205, 1.0 op_sel:[1,0,0]
	v_pk_fma_f32 v[88:89], v[222:223], v[218:219], v[88:89] op_sel:[0,1,0] op_sel_hi:[1,1,1]
	v_cvt_scalef32_pk_f32_fp4 v[224:225], v205, 1.0 op_sel:[0,1,0]
	v_pk_fma_f32 v[86:87], v[224:225], v[218:219], v[86:87] op_sel:[0,1,0] op_sel_hi:[1,1,1]
	v_cvt_scalef32_pk_f32_fp4 v[226:227], v205, 1.0 op_sel:[1,1,0]
	v_pk_fma_f32 v[84:85], v[226:227], v[218:219], v[84:85] op_sel:[0,1,0] op_sel_hi:[1,1,1]
	v_cvt_scalef32_pk_f32_fp4 v[220:221], v206, 1.0
	v_pk_fma_f32 v[82:83], v[220:221], v[218:219], v[82:83] op_sel:[0,1,0] op_sel_hi:[1,1,1]
	v_cvt_scalef32_pk_f32_fp4 v[222:223], v206, 1.0 op_sel:[1,0,0]
	v_pk_fma_f32 v[80:81], v[222:223], v[218:219], v[80:81] op_sel:[0,1,0] op_sel_hi:[1,1,1]
	v_cvt_scalef32_pk_f32_fp4 v[224:225], v206, 1.0 op_sel:[0,1,0]
	v_pk_fma_f32 v[78:79], v[224:225], v[218:219], v[78:79] op_sel:[0,1,0] op_sel_hi:[1,1,1]
	v_cvt_scalef32_pk_f32_fp4 v[226:227], v206, 1.0 op_sel:[1,1,0]
	v_pk_fma_f32 v[76:77], v[226:227], v[218:219], v[76:77] op_sel:[0,1,0] op_sel_hi:[1,1,1]
	v_cvt_scalef32_pk_f32_fp4 v[220:221], v207, 1.0
	v_pk_fma_f32 v[74:75], v[220:221], v[218:219], v[74:75] op_sel:[0,1,0] op_sel_hi:[1,1,1]
	v_cvt_scalef32_pk_f32_fp4 v[222:223], v207, 1.0 op_sel:[1,0,0]
	v_pk_fma_f32 v[72:73], v[222:223], v[218:219], v[72:73] op_sel:[0,1,0] op_sel_hi:[1,1,1]
	v_cvt_scalef32_pk_f32_fp4 v[224:225], v207, 1.0 op_sel:[0,1,0]
	v_pk_fma_f32 v[70:71], v[224:225], v[218:219], v[70:71] op_sel:[0,1,0] op_sel_hi:[1,1,1]
	v_cvt_scalef32_pk_f32_fp4 v[226:227], v207, 1.0 op_sel:[1,1,0]
	v_pk_fma_f32 v[68:69], v[226:227], v[218:219], v[68:69] op_sel:[0,1,0] op_sel_hi:[1,1,1]
	v_cvt_scalef32_pk_f32_fp4 v[220:221], v208, 1.0
	v_pk_fma_f32 v[66:67], v[220:221], v[218:219], v[66:67] op_sel:[0,1,0] op_sel_hi:[1,1,1]
	v_cvt_scalef32_pk_f32_fp4 v[222:223], v208, 1.0 op_sel:[1,0,0]
	v_pk_fma_f32 v[64:65], v[222:223], v[218:219], v[64:65] op_sel:[0,1,0] op_sel_hi:[1,1,1]
	v_cvt_scalef32_pk_f32_fp4 v[224:225], v208, 1.0 op_sel:[0,1,0]
	v_pk_fma_f32 v[62:63], v[224:225], v[218:219], v[62:63] op_sel:[0,1,0] op_sel_hi:[1,1,1]
	v_cvt_scalef32_pk_f32_fp4 v[226:227], v208, 1.0 op_sel:[1,1,0]
	v_pk_fma_f32 v[60:61], v[226:227], v[218:219], v[60:61] op_sel:[0,1,0] op_sel_hi:[1,1,1]
	v_cvt_scalef32_pk_f32_fp4 v[220:221], v209, 1.0
	v_pk_fma_f32 v[58:59], v[220:221], v[218:219], v[58:59] op_sel:[0,1,0] op_sel_hi:[1,1,1]
	v_cvt_scalef32_pk_f32_fp4 v[222:223], v209, 1.0 op_sel:[1,0,0]
	v_pk_fma_f32 v[56:57], v[222:223], v[218:219], v[56:57] op_sel:[0,1,0] op_sel_hi:[1,1,1]
	v_cvt_scalef32_pk_f32_fp4 v[224:225], v209, 1.0 op_sel:[0,1,0]
	v_pk_fma_f32 v[54:55], v[224:225], v[218:219], v[54:55] op_sel:[0,1,0] op_sel_hi:[1,1,1]
	v_cvt_scalef32_pk_f32_fp4 v[226:227], v209, 1.0 op_sel:[1,1,0]
	v_pk_fma_f32 v[52:53], v[226:227], v[218:219], v[52:53] op_sel:[0,1,0] op_sel_hi:[1,1,1]
	v_cvt_scalef32_pk_f32_fp4 v[220:221], v210, 1.0
	v_pk_fma_f32 v[50:51], v[220:221], v[218:219], v[50:51] op_sel:[0,1,0] op_sel_hi:[1,1,1]
	v_cvt_scalef32_pk_f32_fp4 v[222:223], v210, 1.0 op_sel:[1,0,0]
	v_pk_fma_f32 v[46:47], v[222:223], v[218:219], v[46:47] op_sel:[0,1,0] op_sel_hi:[1,1,1]
	v_cvt_scalef32_pk_f32_fp4 v[224:225], v210, 1.0 op_sel:[0,1,0]
	v_pk_fma_f32 v[44:45], v[224:225], v[218:219], v[44:45] op_sel:[0,1,0] op_sel_hi:[1,1,1]
	v_cvt_scalef32_pk_f32_fp4 v[226:227], v210, 1.0 op_sel:[1,1,0]
	v_pk_fma_f32 v[42:43], v[226:227], v[218:219], v[42:43] op_sel:[0,1,0] op_sel_hi:[1,1,1]
	v_cvt_scalef32_pk_f32_fp4 v[220:221], v211, 1.0
	v_pk_fma_f32 v[40:41], v[220:221], v[218:219], v[40:41] op_sel:[0,1,0] op_sel_hi:[1,1,1]
	v_cvt_scalef32_pk_f32_fp4 v[222:223], v211, 1.0 op_sel:[1,0,0]
	v_pk_fma_f32 v[38:39], v[222:223], v[218:219], v[38:39] op_sel:[0,1,0] op_sel_hi:[1,1,1]
	v_cvt_scalef32_pk_f32_fp4 v[224:225], v211, 1.0 op_sel:[0,1,0]
	v_pk_fma_f32 v[36:37], v[224:225], v[218:219], v[36:37] op_sel:[0,1,0] op_sel_hi:[1,1,1]
	v_cvt_scalef32_pk_f32_fp4 v[226:227], v211, 1.0 op_sel:[1,1,0]
	v_pk_fma_f32 v[34:35], v[226:227], v[218:219], v[34:35] op_sel:[0,1,0] op_sel_hi:[1,1,1]
	v_readfirstlane_b32 s60, v212
	v_readfirstlane_b32 s61, v213
	v_readfirstlane_b32 s62, v214
	v_readfirstlane_b32 s63, v215
	s_lshl_b32 s60, s60, 11
	v_add_u32_e32 v101, s60, v100
	global_load_dwordx4 v[180:183], v101, s[58:59]
	global_load_dwordx4 v[184:187], v101, s[58:59] offset:1024
	s_lshl_b32 s61, s61, 11
	v_add_u32_e32 v101, s61, v100
	global_load_dwordx4 v[188:191], v101, s[58:59]
	global_load_dwordx4 v[192:195], v101, s[58:59] offset:1024
	s_lshl_b32 s62, s62, 11
	v_add_u32_e32 v101, s62, v100
	global_load_dwordx4 v[196:199], v101, s[58:59]
	global_load_dwordx4 v[200:203], v101, s[58:59] offset:1024
	s_lshl_b32 s63, s63, 11
	v_add_u32_e32 v101, s63, v100
	global_load_dwordx4 v[204:207], v101, s[58:59]
	global_load_dwordx4 v[208:211], v101, s[58:59] offset:1024
	v_add_u32_e32 v102, 32, v102
	s_add_u32 s10, s10, 1
	s_cmp_lt_u32 s10, 15
	s_cbranch_scc1 .Lpv_loop
	ds_read_b128 v[216:219], v102 offset:512
	s_waitcnt lgkmcnt(0)
	s_waitcnt vmcnt(14)
	v_cvt_scalef32_pk_f32_fp4 v[220:221], v148, 1.0
	v_pk_fma_f32 v[96:97], v[220:221], v[216:217], v[96:97] op_sel_hi:[1,0,1]
	v_cvt_scalef32_pk_f32_fp4 v[222:223], v148, 1.0 op_sel:[1,0,0]
	v_pk_fma_f32 v[98:99], v[222:223], v[216:217], v[98:99] op_sel_hi:[1,0,1]
	v_cvt_scalef32_pk_f32_fp4 v[224:225], v148, 1.0 op_sel:[0,1,0]
	v_pk_fma_f32 v[94:95], v[224:225], v[216:217], v[94:95] op_sel_hi:[1,0,1]
	v_cvt_scalef32_pk_f32_fp4 v[226:227], v148, 1.0 op_sel:[1,1,0]
	v_pk_fma_f32 v[92:93], v[226:227], v[216:217], v[92:93] op_sel_hi:[1,0,1]
	v_cvt_scalef32_pk_f32_fp4 v[220:221], v149, 1.0
	v_pk_fma_f32 v[90:91], v[220:221], v[216:217], v[90:91] op_sel_hi:[1,0,1]
	v_cvt_scalef32_pk_f32_fp4 v[222:223], v149, 1.0 op_sel:[1,0,0]
	v_pk_fma_f32 v[88:89], v[222:223], v[216:217], v[88:89] op_sel_hi:[1,0,1]
	v_cvt_scalef32_pk_f32_fp4 v[224:225], v149, 1.0 op_sel:[0,1,0]
	v_pk_fma_f32 v[86:87], v[224:225], v[216:217], v[86:87] op_sel_hi:[1,0,1]
	v_cvt_scalef32_pk_f32_fp4 v[226:227], v149, 1.0 op_sel:[1,1,0]
	v_pk_fma_f32 v[84:85], v[226:227], v[216:217], v[84:85] op_sel_hi:[1,0,1]
	v_cvt_scalef32_pk_f32_fp4 v[220:221], v150, 1.0
	v_pk_fma_f32 v[82:83], v[220:221], v[216:217], v[82:83] op_sel_hi:[1,0,1]
	v_cvt_scalef32_pk_f32_fp4 v[222:223], v150, 1.0 op_sel:[1,0,0]
	v_pk_fma_f32 v[80:81], v[222:223], v[216:217], v[80:81] op_sel_hi:[1,0,1]
	v_cvt_scalef32_pk_f32_fp4 v[224:225], v150, 1.0 op_sel:[0,1,0]
	v_pk_fma_f32 v[78:79], v[224:225], v[216:217], v[78:79] op_sel_hi:[1,0,1]
	v_cvt_scalef32_pk_f32_fp4 v[226:227], v150, 1.0 op_sel:[1,1,0]
	v_pk_fma_f32 v[76:77], v[226:227], v[216:217], v[76:77] op_sel_hi:[1,0,1]
	v_cvt_scalef32_pk_f32_fp4 v[220:221], v151, 1.0
	v_pk_fma_f32 v[74:75], v[220:221], v[216:217], v[74:75] op_sel_hi:[1,0,1]
	v_cvt_scalef32_pk_f32_fp4 v[222:223], v151, 1.0 op_sel:[1,0,0]
	v_pk_fma_f32 v[72:73], v[222:223], v[216:217], v[72:73] op_sel_hi:[1,0,1]
	v_cvt_scalef32_pk_f32_fp4 v[224:225], v151, 1.0 op_sel:[0,1,0]
	v_pk_fma_f32 v[70:71], v[224:225], v[216:217], v[70:71] op_sel_hi:[1,0,1]
	v_cvt_scalef32_pk_f32_fp4 v[226:227], v151, 1.0 op_sel:[1,1,0]
	v_pk_fma_f32 v[68:69], v[226:227], v[216:217], v[68:69] op_sel_hi:[1,0,1]
	v_cvt_scalef32_pk_f32_fp4 v[220:221], v152, 1.0
	v_pk_fma_f32 v[66:67], v[220:221], v[216:217], v[66:67] op_sel_hi:[1,0,1]
	v_cvt_scalef32_pk_f32_fp4 v[222:223], v152, 1.0 op_sel:[1,0,0]
	v_pk_fma_f32 v[64:65], v[222:223], v[216:217], v[64:65] op_sel_hi:[1,0,1]
	v_cvt_scalef32_pk_f32_fp4 v[224:225], v152, 1.0 op_sel:[0,1,0]
	v_pk_fma_f32 v[62:63], v[224:225], v[216:217], v[62:63] op_sel_hi:[1,0,1]
	v_cvt_scalef32_pk_f32_fp4 v[226:227], v152, 1.0 op_sel:[1,1,0]
	v_pk_fma_f32 v[60:61], v[226:227], v[216:217], v[60:61] op_sel_hi:[1,0,1]
	v_cvt_scalef32_pk_f32_fp4 v[220:221], v153, 1.0
	v_pk_fma_f32 v[58:59], v[220:221], v[216:217], v[58:59] op_sel_hi:[1,0,1]
	v_cvt_scalef32_pk_f32_fp4 v[222:223], v153, 1.0 op_sel:[1,0,0]
	v_pk_fma_f32 v[56:57], v[222:223], v[216:217], v[56:57] op_sel_hi:[1,0,1]
	v_cvt_scalef32_pk_f32_fp4 v[224:225], v153, 1.0 op_sel:[0,1,0]
	v_pk_fma_f32 v[54:55], v[224:225], v[216:217], v[54:55] op_sel_hi:[1,0,1]
	v_cvt_scalef32_pk_f32_fp4 v[226:227], v153, 1.0 op_sel:[1,1,0]
	v_pk_fma_f32 v[52:53], v[226:227], v[216:217], v[52:53] op_sel_hi:[1,0,1]
	v_cvt_scalef32_pk_f32_fp4 v[220:221], v154, 1.0
	v_pk_fma_f32 v[50:51], v[220:221], v[216:217], v[50:51] op_sel_hi:[1,0,1]
	v_cvt_scalef32_pk_f32_fp4 v[222:223], v154, 1.0 op_sel:[1,0,0]
	v_pk_fma_f32 v[46:47], v[222:223], v[216:217], v[46:47] op_sel_hi:[1,0,1]
	v_cvt_scalef32_pk_f32_fp4 v[224:225], v154, 1.0 op_sel:[0,1,0]
	v_pk_fma_f32 v[44:45], v[224:225], v[216:217], v[44:45] op_sel_hi:[1,0,1]
	v_cvt_scalef32_pk_f32_fp4 v[226:227], v154, 1.0 op_sel:[1,1,0]
	v_pk_fma_f32 v[42:43], v[226:227], v[216:217], v[42:43] op_sel_hi:[1,0,1]
	v_cvt_scalef32_pk_f32_fp4 v[220:221], v155, 1.0
	v_pk_fma_f32 v[40:41], v[220:221], v[216:217], v[40:41] op_sel_hi:[1,0,1]
	v_cvt_scalef32_pk_f32_fp4 v[222:223], v155, 1.0 op_sel:[1,0,0]
	v_pk_fma_f32 v[38:39], v[222:223], v[216:217], v[38:39] op_sel_hi:[1,0,1]
	v_cvt_scalef32_pk_f32_fp4 v[224:225], v155, 1.0 op_sel:[0,1,0]
	v_pk_fma_f32 v[36:37], v[224:225], v[216:217], v[36:37] op_sel_hi:[1,0,1]
	v_cvt_scalef32_pk_f32_fp4 v[226:227], v155, 1.0 op_sel:[1,1,0]
	v_pk_fma_f32 v[34:35], v[226:227], v[216:217], v[34:35] op_sel_hi:[1,0,1]
	s_waitcnt vmcnt(12)
	v_cvt_scalef32_pk_f32_fp4 v[220:221], v156, 1.0
	v_pk_fma_f32 v[96:97], v[220:221], v[216:217], v[96:97] op_sel:[0,1,0] op_sel_hi:[1,1,1]
	v_cvt_scalef32_pk_f32_fp4 v[222:223], v156, 1.0 op_sel:[1,0,0]
	v_pk_fma_f32 v[98:99], v[222:223], v[216:217], v[98:99] op_sel:[0,1,0] op_sel_hi:[1,1,1]
	v_cvt_scalef32_pk_f32_fp4 v[224:225], v156, 1.0 op_sel:[0,1,0]
	v_pk_fma_f32 v[94:95], v[224:225], v[216:217], v[94:95] op_sel:[0,1,0] op_sel_hi:[1,1,1]
	v_cvt_scalef32_pk_f32_fp4 v[226:227], v156, 1.0 op_sel:[1,1,0]
	v_pk_fma_f32 v[92:93], v[226:227], v[216:217], v[92:93] op_sel:[0,1,0] op_sel_hi:[1,1,1]
	v_cvt_scalef32_pk_f32_fp4 v[220:221], v157, 1.0
	v_pk_fma_f32 v[90:91], v[220:221], v[216:217], v[90:91] op_sel:[0,1,0] op_sel_hi:[1,1,1]
	v_cvt_scalef32_pk_f32_fp4 v[222:223], v157, 1.0 op_sel:[1,0,0]
	v_pk_fma_f32 v[88:89], v[222:223], v[216:217], v[88:89] op_sel:[0,1,0] op_sel_hi:[1,1,1]
	v_cvt_scalef32_pk_f32_fp4 v[224:225], v157, 1.0 op_sel:[0,1,0]
	v_pk_fma_f32 v[86:87], v[224:225], v[216:217], v[86:87] op_sel:[0,1,0] op_sel_hi:[1,1,1]
	v_cvt_scalef32_pk_f32_fp4 v[226:227], v157, 1.0 op_sel:[1,1,0]
	v_pk_fma_f32 v[84:85], v[226:227], v[216:217], v[84:85] op_sel:[0,1,0] op_sel_hi:[1,1,1]
	v_cvt_scalef32_pk_f32_fp4 v[220:221], v158, 1.0
	v_pk_fma_f32 v[82:83], v[220:221], v[216:217], v[82:83] op_sel:[0,1,0] op_sel_hi:[1,1,1]
	v_cvt_scalef32_pk_f32_fp4 v[222:223], v158, 1.0 op_sel:[1,0,0]
	v_pk_fma_f32 v[80:81], v[222:223], v[216:217], v[80:81] op_sel:[0,1,0] op_sel_hi:[1,1,1]
	v_cvt_scalef32_pk_f32_fp4 v[224:225], v158, 1.0 op_sel:[0,1,0]
	v_pk_fma_f32 v[78:79], v[224:225], v[216:217], v[78:79] op_sel:[0,1,0] op_sel_hi:[1,1,1]
	v_cvt_scalef32_pk_f32_fp4 v[226:227], v158, 1.0 op_sel:[1,1,0]
	v_pk_fma_f32 v[76:77], v[226:227], v[216:217], v[76:77] op_sel:[0,1,0] op_sel_hi:[1,1,1]
	v_cvt_scalef32_pk_f32_fp4 v[220:221], v159, 1.0
	v_pk_fma_f32 v[74:75], v[220:221], v[216:217], v[74:75] op_sel:[0,1,0] op_sel_hi:[1,1,1]
	v_cvt_scalef32_pk_f32_fp4 v[222:223], v159, 1.0 op_sel:[1,0,0]
	v_pk_fma_f32 v[72:73], v[222:223], v[216:217], v[72:73] op_sel:[0,1,0] op_sel_hi:[1,1,1]
	v_cvt_scalef32_pk_f32_fp4 v[224:225], v159, 1.0 op_sel:[0,1,0]
	v_pk_fma_f32 v[70:71], v[224:225], v[216:217], v[70:71] op_sel:[0,1,0] op_sel_hi:[1,1,1]
	v_cvt_scalef32_pk_f32_fp4 v[226:227], v159, 1.0 op_sel:[1,1,0]
	v_pk_fma_f32 v[68:69], v[226:227], v[216:217], v[68:69] op_sel:[0,1,0] op_sel_hi:[1,1,1]
	v_cvt_scalef32_pk_f32_fp4 v[220:221], v160, 1.0
	v_pk_fma_f32 v[66:67], v[220:221], v[216:217], v[66:67] op_sel:[0,1,0] op_sel_hi:[1,1,1]
	v_cvt_scalef32_pk_f32_fp4 v[222:223], v160, 1.0 op_sel:[1,0,0]
	v_pk_fma_f32 v[64:65], v[222:223], v[216:217], v[64:65] op_sel:[0,1,0] op_sel_hi:[1,1,1]
	v_cvt_scalef32_pk_f32_fp4 v[224:225], v160, 1.0 op_sel:[0,1,0]
	v_pk_fma_f32 v[62:63], v[224:225], v[216:217], v[62:63] op_sel:[0,1,0] op_sel_hi:[1,1,1]
	v_cvt_scalef32_pk_f32_fp4 v[226:227], v160, 1.0 op_sel:[1,1,0]
	v_pk_fma_f32 v[60:61], v[226:227], v[216:217], v[60:61] op_sel:[0,1,0] op_sel_hi:[1,1,1]
	v_cvt_scalef32_pk_f32_fp4 v[220:221], v161, 1.0
	v_pk_fma_f32 v[58:59], v[220:221], v[216:217], v[58:59] op_sel:[0,1,0] op_sel_hi:[1,1,1]
	v_cvt_scalef32_pk_f32_fp4 v[222:223], v161, 1.0 op_sel:[1,0,0]
	v_pk_fma_f32 v[56:57], v[222:223], v[216:217], v[56:57] op_sel:[0,1,0] op_sel_hi:[1,1,1]
	v_cvt_scalef32_pk_f32_fp4 v[224:225], v161, 1.0 op_sel:[0,1,0]
	v_pk_fma_f32 v[54:55], v[224:225], v[216:217], v[54:55] op_sel:[0,1,0] op_sel_hi:[1,1,1]
	v_cvt_scalef32_pk_f32_fp4 v[226:227], v161, 1.0 op_sel:[1,1,0]
	v_pk_fma_f32 v[52:53], v[226:227], v[216:217], v[52:53] op_sel:[0,1,0] op_sel_hi:[1,1,1]
	v_cvt_scalef32_pk_f32_fp4 v[220:221], v162, 1.0
	v_pk_fma_f32 v[50:51], v[220:221], v[216:217], v[50:51] op_sel:[0,1,0] op_sel_hi:[1,1,1]
	v_cvt_scalef32_pk_f32_fp4 v[222:223], v162, 1.0 op_sel:[1,0,0]
	v_pk_fma_f32 v[46:47], v[222:223], v[216:217], v[46:47] op_sel:[0,1,0] op_sel_hi:[1,1,1]
	v_cvt_scalef32_pk_f32_fp4 v[224:225], v162, 1.0 op_sel:[0,1,0]
	v_pk_fma_f32 v[44:45], v[224:225], v[216:217], v[44:45] op_sel:[0,1,0] op_sel_hi:[1,1,1]
	v_cvt_scalef32_pk_f32_fp4 v[226:227], v162, 1.0 op_sel:[1,1,0]
	v_pk_fma_f32 v[42:43], v[226:227], v[216:217], v[42:43] op_sel:[0,1,0] op_sel_hi:[1,1,1]
	v_cvt_scalef32_pk_f32_fp4 v[220:221], v163, 1.0
	v_pk_fma_f32 v[40:41], v[220:221], v[216:217], v[40:41] op_sel:[0,1,0] op_sel_hi:[1,1,1]
	v_cvt_scalef32_pk_f32_fp4 v[222:223], v163, 1.0 op_sel:[1,0,0]
	v_pk_fma_f32 v[38:39], v[222:223], v[216:217], v[38:39] op_sel:[0,1,0] op_sel_hi:[1,1,1]
	v_cvt_scalef32_pk_f32_fp4 v[224:225], v163, 1.0 op_sel:[0,1,0]
	v_pk_fma_f32 v[36:37], v[224:225], v[216:217], v[36:37] op_sel:[0,1,0] op_sel_hi:[1,1,1]
	v_cvt_scalef32_pk_f32_fp4 v[226:227], v163, 1.0 op_sel:[1,1,0]
	v_pk_fma_f32 v[34:35], v[226:227], v[216:217], v[34:35] op_sel:[0,1,0] op_sel_hi:[1,1,1]
	s_waitcnt vmcnt(10)
	v_cvt_scalef32_pk_f32_fp4 v[220:221], v164, 1.0
	v_pk_fma_f32 v[96:97], v[220:221], v[218:219], v[96:97] op_sel_hi:[1,0,1]
	v_cvt_scalef32_pk_f32_fp4 v[222:223], v164, 1.0 op_sel:[1,0,0]
	v_pk_fma_f32 v[98:99], v[222:223], v[218:219], v[98:99] op_sel_hi:[1,0,1]
	v_cvt_scalef32_pk_f32_fp4 v[224:225], v164, 1.0 op_sel:[0,1,0]
	v_pk_fma_f32 v[94:95], v[224:225], v[218:219], v[94:95] op_sel_hi:[1,0,1]
	v_cvt_scalef32_pk_f32_fp4 v[226:227], v164, 1.0 op_sel:[1,1,0]
	v_pk_fma_f32 v[92:93], v[226:227], v[218:219], v[92:93] op_sel_hi:[1,0,1]
	v_cvt_scalef32_pk_f32_fp4 v[220:221], v165, 1.0
	v_pk_fma_f32 v[90:91], v[220:221], v[218:219], v[90:91] op_sel_hi:[1,0,1]
	v_cvt_scalef32_pk_f32_fp4 v[222:223], v165, 1.0 op_sel:[1,0,0]
	v_pk_fma_f32 v[88:89], v[222:223], v[218:219], v[88:89] op_sel_hi:[1,0,1]
	v_cvt_scalef32_pk_f32_fp4 v[224:225], v165, 1.0 op_sel:[0,1,0]
	v_pk_fma_f32 v[86:87], v[224:225], v[218:219], v[86:87] op_sel_hi:[1,0,1]
	v_cvt_scalef32_pk_f32_fp4 v[226:227], v165, 1.0 op_sel:[1,1,0]
	v_pk_fma_f32 v[84:85], v[226:227], v[218:219], v[84:85] op_sel_hi:[1,0,1]
	v_cvt_scalef32_pk_f32_fp4 v[220:221], v166, 1.0
	v_pk_fma_f32 v[82:83], v[220:221], v[218:219], v[82:83] op_sel_hi:[1,0,1]
	v_cvt_scalef32_pk_f32_fp4 v[222:223], v166, 1.0 op_sel:[1,0,0]
	v_pk_fma_f32 v[80:81], v[222:223], v[218:219], v[80:81] op_sel_hi:[1,0,1]
	v_cvt_scalef32_pk_f32_fp4 v[224:225], v166, 1.0 op_sel:[0,1,0]
	v_pk_fma_f32 v[78:79], v[224:225], v[218:219], v[78:79] op_sel_hi:[1,0,1]
	v_cvt_scalef32_pk_f32_fp4 v[226:227], v166, 1.0 op_sel:[1,1,0]
	v_pk_fma_f32 v[76:77], v[226:227], v[218:219], v[76:77] op_sel_hi:[1,0,1]
	v_cvt_scalef32_pk_f32_fp4 v[220:221], v167, 1.0
	v_pk_fma_f32 v[74:75], v[220:221], v[218:219], v[74:75] op_sel_hi:[1,0,1]
	v_cvt_scalef32_pk_f32_fp4 v[222:223], v167, 1.0 op_sel:[1,0,0]
	v_pk_fma_f32 v[72:73], v[222:223], v[218:219], v[72:73] op_sel_hi:[1,0,1]
	v_cvt_scalef32_pk_f32_fp4 v[224:225], v167, 1.0 op_sel:[0,1,0]
	v_pk_fma_f32 v[70:71], v[224:225], v[218:219], v[70:71] op_sel_hi:[1,0,1]
	v_cvt_scalef32_pk_f32_fp4 v[226:227], v167, 1.0 op_sel:[1,1,0]
	v_pk_fma_f32 v[68:69], v[226:227], v[218:219], v[68:69] op_sel_hi:[1,0,1]
	v_cvt_scalef32_pk_f32_fp4 v[220:221], v168, 1.0
	v_pk_fma_f32 v[66:67], v[220:221], v[218:219], v[66:67] op_sel_hi:[1,0,1]
	v_cvt_scalef32_pk_f32_fp4 v[222:223], v168, 1.0 op_sel:[1,0,0]
	v_pk_fma_f32 v[64:65], v[222:223], v[218:219], v[64:65] op_sel_hi:[1,0,1]
	v_cvt_scalef32_pk_f32_fp4 v[224:225], v168, 1.0 op_sel:[0,1,0]
	v_pk_fma_f32 v[62:63], v[224:225], v[218:219], v[62:63] op_sel_hi:[1,0,1]
	v_cvt_scalef32_pk_f32_fp4 v[226:227], v168, 1.0 op_sel:[1,1,0]
	v_pk_fma_f32 v[60:61], v[226:227], v[218:219], v[60:61] op_sel_hi:[1,0,1]
	v_cvt_scalef32_pk_f32_fp4 v[220:221], v169, 1.0
	v_pk_fma_f32 v[58:59], v[220:221], v[218:219], v[58:59] op_sel_hi:[1,0,1]
	v_cvt_scalef32_pk_f32_fp4 v[222:223], v169, 1.0 op_sel:[1,0,0]
	v_pk_fma_f32 v[56:57], v[222:223], v[218:219], v[56:57] op_sel_hi:[1,0,1]
	v_cvt_scalef32_pk_f32_fp4 v[224:225], v169, 1.0 op_sel:[0,1,0]
	v_pk_fma_f32 v[54:55], v[224:225], v[218:219], v[54:55] op_sel_hi:[1,0,1]
	v_cvt_scalef32_pk_f32_fp4 v[226:227], v169, 1.0 op_sel:[1,1,0]
	v_pk_fma_f32 v[52:53], v[226:227], v[218:219], v[52:53] op_sel_hi:[1,0,1]
	v_cvt_scalef32_pk_f32_fp4 v[220:221], v170, 1.0
	v_pk_fma_f32 v[50:51], v[220:221], v[218:219], v[50:51] op_sel_hi:[1,0,1]
	v_cvt_scalef32_pk_f32_fp4 v[222:223], v170, 1.0 op_sel:[1,0,0]
	v_pk_fma_f32 v[46:47], v[222:223], v[218:219], v[46:47] op_sel_hi:[1,0,1]
	v_cvt_scalef32_pk_f32_fp4 v[224:225], v170, 1.0 op_sel:[0,1,0]
	v_pk_fma_f32 v[44:45], v[224:225], v[218:219], v[44:45] op_sel_hi:[1,0,1]
	v_cvt_scalef32_pk_f32_fp4 v[226:227], v170, 1.0 op_sel:[1,1,0]
	v_pk_fma_f32 v[42:43], v[226:227], v[218:219], v[42:43] op_sel_hi:[1,0,1]
	v_cvt_scalef32_pk_f32_fp4 v[220:221], v171, 1.0
	v_pk_fma_f32 v[40:41], v[220:221], v[218:219], v[40:41] op_sel_hi:[1,0,1]
	v_cvt_scalef32_pk_f32_fp4 v[222:223], v171, 1.0 op_sel:[1,0,0]
	v_pk_fma_f32 v[38:39], v[222:223], v[218:219], v[38:39] op_sel_hi:[1,0,1]
	v_cvt_scalef32_pk_f32_fp4 v[224:225], v171, 1.0 op_sel:[0,1,0]
	v_pk_fma_f32 v[36:37], v[224:225], v[218:219], v[36:37] op_sel_hi:[1,0,1]
	v_cvt_scalef32_pk_f32_fp4 v[226:227], v171, 1.0 op_sel:[1,1,0]
	v_pk_fma_f32 v[34:35], v[226:227], v[218:219], v[34:35] op_sel_hi:[1,0,1]
	s_waitcnt vmcnt(8)
	v_cvt_scalef32_pk_f32_fp4 v[220:221], v172, 1.0
	v_pk_fma_f32 v[96:97], v[220:221], v[218:219], v[96:97] op_sel:[0,1,0] op_sel_hi:[1,1,1]
	v_cvt_scalef32_pk_f32_fp4 v[222:223], v172, 1.0 op_sel:[1,0,0]
	v_pk_fma_f32 v[98:99], v[222:223], v[218:219], v[98:99] op_sel:[0,1,0] op_sel_hi:[1,1,1]
	v_cvt_scalef32_pk_f32_fp4 v[224:225], v172, 1.0 op_sel:[0,1,0]
	v_pk_fma_f32 v[94:95], v[224:225], v[218:219], v[94:95] op_sel:[0,1,0] op_sel_hi:[1,1,1]
	v_cvt_scalef32_pk_f32_fp4 v[226:227], v172, 1.0 op_sel:[1,1,0]
	v_pk_fma_f32 v[92:93], v[226:227], v[218:219], v[92:93] op_sel:[0,1,0] op_sel_hi:[1,1,1]
	v_cvt_scalef32_pk_f32_fp4 v[220:221], v173, 1.0
	v_pk_fma_f32 v[90:91], v[220:221], v[218:219], v[90:91] op_sel:[0,1,0] op_sel_hi:[1,1,1]
	v_cvt_scalef32_pk_f32_fp4 v[222:223], v173, 1.0 op_sel:[1,0,0]
	v_pk_fma_f32 v[88:89], v[222:223], v[218:219], v[88:89] op_sel:[0,1,0] op_sel_hi:[1,1,1]
	v_cvt_scalef32_pk_f32_fp4 v[224:225], v173, 1.0 op_sel:[0,1,0]
	v_pk_fma_f32 v[86:87], v[224:225], v[218:219], v[86:87] op_sel:[0,1,0] op_sel_hi:[1,1,1]
	v_cvt_scalef32_pk_f32_fp4 v[226:227], v173, 1.0 op_sel:[1,1,0]
	v_pk_fma_f32 v[84:85], v[226:227], v[218:219], v[84:85] op_sel:[0,1,0] op_sel_hi:[1,1,1]
	v_cvt_scalef32_pk_f32_fp4 v[220:221], v174, 1.0
	v_pk_fma_f32 v[82:83], v[220:221], v[218:219], v[82:83] op_sel:[0,1,0] op_sel_hi:[1,1,1]
	v_cvt_scalef32_pk_f32_fp4 v[222:223], v174, 1.0 op_sel:[1,0,0]
	v_pk_fma_f32 v[80:81], v[222:223], v[218:219], v[80:81] op_sel:[0,1,0] op_sel_hi:[1,1,1]
	v_cvt_scalef32_pk_f32_fp4 v[224:225], v174, 1.0 op_sel:[0,1,0]
	v_pk_fma_f32 v[78:79], v[224:225], v[218:219], v[78:79] op_sel:[0,1,0] op_sel_hi:[1,1,1]
	v_cvt_scalef32_pk_f32_fp4 v[226:227], v174, 1.0 op_sel:[1,1,0]
	v_pk_fma_f32 v[76:77], v[226:227], v[218:219], v[76:77] op_sel:[0,1,0] op_sel_hi:[1,1,1]
	v_cvt_scalef32_pk_f32_fp4 v[220:221], v175, 1.0
	v_pk_fma_f32 v[74:75], v[220:221], v[218:219], v[74:75] op_sel:[0,1,0] op_sel_hi:[1,1,1]
	v_cvt_scalef32_pk_f32_fp4 v[222:223], v175, 1.0 op_sel:[1,0,0]
	v_pk_fma_f32 v[72:73], v[222:223], v[218:219], v[72:73] op_sel:[0,1,0] op_sel_hi:[1,1,1]
	v_cvt_scalef32_pk_f32_fp4 v[224:225], v175, 1.0 op_sel:[0,1,0]
	v_pk_fma_f32 v[70:71], v[224:225], v[218:219], v[70:71] op_sel:[0,1,0] op_sel_hi:[1,1,1]
	v_cvt_scalef32_pk_f32_fp4 v[226:227], v175, 1.0 op_sel:[1,1,0]
	v_pk_fma_f32 v[68:69], v[226:227], v[218:219], v[68:69] op_sel:[0,1,0] op_sel_hi:[1,1,1]
	v_cvt_scalef32_pk_f32_fp4 v[220:221], v176, 1.0
	v_pk_fma_f32 v[66:67], v[220:221], v[218:219], v[66:67] op_sel:[0,1,0] op_sel_hi:[1,1,1]
	v_cvt_scalef32_pk_f32_fp4 v[222:223], v176, 1.0 op_sel:[1,0,0]
	v_pk_fma_f32 v[64:65], v[222:223], v[218:219], v[64:65] op_sel:[0,1,0] op_sel_hi:[1,1,1]
	v_cvt_scalef32_pk_f32_fp4 v[224:225], v176, 1.0 op_sel:[0,1,0]
	v_pk_fma_f32 v[62:63], v[224:225], v[218:219], v[62:63] op_sel:[0,1,0] op_sel_hi:[1,1,1]
	v_cvt_scalef32_pk_f32_fp4 v[226:227], v176, 1.0 op_sel:[1,1,0]
	v_pk_fma_f32 v[60:61], v[226:227], v[218:219], v[60:61] op_sel:[0,1,0] op_sel_hi:[1,1,1]
	v_cvt_scalef32_pk_f32_fp4 v[220:221], v177, 1.0
	v_pk_fma_f32 v[58:59], v[220:221], v[218:219], v[58:59] op_sel:[0,1,0] op_sel_hi:[1,1,1]
	v_cvt_scalef32_pk_f32_fp4 v[222:223], v177, 1.0 op_sel:[1,0,0]
	v_pk_fma_f32 v[56:57], v[222:223], v[218:219], v[56:57] op_sel:[0,1,0] op_sel_hi:[1,1,1]
	v_cvt_scalef32_pk_f32_fp4 v[224:225], v177, 1.0 op_sel:[0,1,0]
	v_pk_fma_f32 v[54:55], v[224:225], v[218:219], v[54:55] op_sel:[0,1,0] op_sel_hi:[1,1,1]
	v_cvt_scalef32_pk_f32_fp4 v[226:227], v177, 1.0 op_sel:[1,1,0]
	v_pk_fma_f32 v[52:53], v[226:227], v[218:219], v[52:53] op_sel:[0,1,0] op_sel_hi:[1,1,1]
	v_cvt_scalef32_pk_f32_fp4 v[220:221], v178, 1.0
	v_pk_fma_f32 v[50:51], v[220:221], v[218:219], v[50:51] op_sel:[0,1,0] op_sel_hi:[1,1,1]
	v_cvt_scalef32_pk_f32_fp4 v[222:223], v178, 1.0 op_sel:[1,0,0]
	v_pk_fma_f32 v[46:47], v[222:223], v[218:219], v[46:47] op_sel:[0,1,0] op_sel_hi:[1,1,1]
	v_cvt_scalef32_pk_f32_fp4 v[224:225], v178, 1.0 op_sel:[0,1,0]
	v_pk_fma_f32 v[44:45], v[224:225], v[218:219], v[44:45] op_sel:[0,1,0] op_sel_hi:[1,1,1]
	v_cvt_scalef32_pk_f32_fp4 v[226:227], v178, 1.0 op_sel:[1,1,0]
	v_pk_fma_f32 v[42:43], v[226:227], v[218:219], v[42:43] op_sel:[0,1,0] op_sel_hi:[1,1,1]
	v_cvt_scalef32_pk_f32_fp4 v[220:221], v179, 1.0
	v_pk_fma_f32 v[40:41], v[220:221], v[218:219], v[40:41] op_sel:[0,1,0] op_sel_hi:[1,1,1]
	v_cvt_scalef32_pk_f32_fp4 v[222:223], v179, 1.0 op_sel:[1,0,0]
	v_pk_fma_f32 v[38:39], v[222:223], v[218:219], v[38:39] op_sel:[0,1,0] op_sel_hi:[1,1,1]
	v_cvt_scalef32_pk_f32_fp4 v[224:225], v179, 1.0 op_sel:[0,1,0]
	v_pk_fma_f32 v[36:37], v[224:225], v[218:219], v[36:37] op_sel:[0,1,0] op_sel_hi:[1,1,1]
	v_cvt_scalef32_pk_f32_fp4 v[226:227], v179, 1.0 op_sel:[1,1,0]
	v_pk_fma_f32 v[34:35], v[226:227], v[218:219], v[34:35] op_sel:[0,1,0] op_sel_hi:[1,1,1]
	ds_read_b128 v[216:219], v102 offset:528
	s_waitcnt lgkmcnt(0)
	s_waitcnt vmcnt(6)
	v_cvt_scalef32_pk_f32_fp4 v[220:221], v180, 1.0
	v_pk_fma_f32 v[96:97], v[220:221], v[216:217], v[96:97] op_sel_hi:[1,0,1]
	v_cvt_scalef32_pk_f32_fp4 v[222:223], v180, 1.0 op_sel:[1,0,0]
	v_pk_fma_f32 v[98:99], v[222:223], v[216:217], v[98:99] op_sel_hi:[1,0,1]
	v_cvt_scalef32_pk_f32_fp4 v[224:225], v180, 1.0 op_sel:[0,1,0]
	v_pk_fma_f32 v[94:95], v[224:225], v[216:217], v[94:95] op_sel_hi:[1,0,1]
	v_cvt_scalef32_pk_f32_fp4 v[226:227], v180, 1.0 op_sel:[1,1,0]
	v_pk_fma_f32 v[92:93], v[226:227], v[216:217], v[92:93] op_sel_hi:[1,0,1]
	v_cvt_scalef32_pk_f32_fp4 v[220:221], v181, 1.0
	v_pk_fma_f32 v[90:91], v[220:221], v[216:217], v[90:91] op_sel_hi:[1,0,1]
	v_cvt_scalef32_pk_f32_fp4 v[222:223], v181, 1.0 op_sel:[1,0,0]
	v_pk_fma_f32 v[88:89], v[222:223], v[216:217], v[88:89] op_sel_hi:[1,0,1]
	v_cvt_scalef32_pk_f32_fp4 v[224:225], v181, 1.0 op_sel:[0,1,0]
	v_pk_fma_f32 v[86:87], v[224:225], v[216:217], v[86:87] op_sel_hi:[1,0,1]
	v_cvt_scalef32_pk_f32_fp4 v[226:227], v181, 1.0 op_sel:[1,1,0]
	v_pk_fma_f32 v[84:85], v[226:227], v[216:217], v[84:85] op_sel_hi:[1,0,1]
	v_cvt_scalef32_pk_f32_fp4 v[220:221], v182, 1.0
	v_pk_fma_f32 v[82:83], v[220:221], v[216:217], v[82:83] op_sel_hi:[1,0,1]
	v_cvt_scalef32_pk_f32_fp4 v[222:223], v182, 1.0 op_sel:[1,0,0]
	v_pk_fma_f32 v[80:81], v[222:223], v[216:217], v[80:81] op_sel_hi:[1,0,1]
	v_cvt_scalef32_pk_f32_fp4 v[224:225], v182, 1.0 op_sel:[0,1,0]
	v_pk_fma_f32 v[78:79], v[224:225], v[216:217], v[78:79] op_sel_hi:[1,0,1]
	v_cvt_scalef32_pk_f32_fp4 v[226:227], v182, 1.0 op_sel:[1,1,0]
	v_pk_fma_f32 v[76:77], v[226:227], v[216:217], v[76:77] op_sel_hi:[1,0,1]
	v_cvt_scalef32_pk_f32_fp4 v[220:221], v183, 1.0
	v_pk_fma_f32 v[74:75], v[220:221], v[216:217], v[74:75] op_sel_hi:[1,0,1]
	v_cvt_scalef32_pk_f32_fp4 v[222:223], v183, 1.0 op_sel:[1,0,0]
	v_pk_fma_f32 v[72:73], v[222:223], v[216:217], v[72:73] op_sel_hi:[1,0,1]
	v_cvt_scalef32_pk_f32_fp4 v[224:225], v183, 1.0 op_sel:[0,1,0]
	v_pk_fma_f32 v[70:71], v[224:225], v[216:217], v[70:71] op_sel_hi:[1,0,1]
	v_cvt_scalef32_pk_f32_fp4 v[226:227], v183, 1.0 op_sel:[1,1,0]
	v_pk_fma_f32 v[68:69], v[226:227], v[216:217], v[68:69] op_sel_hi:[1,0,1]
	v_cvt_scalef32_pk_f32_fp4 v[220:221], v184, 1.0
	v_pk_fma_f32 v[66:67], v[220:221], v[216:217], v[66:67] op_sel_hi:[1,0,1]
	v_cvt_scalef32_pk_f32_fp4 v[222:223], v184, 1.0 op_sel:[1,0,0]
	v_pk_fma_f32 v[64:65], v[222:223], v[216:217], v[64:65] op_sel_hi:[1,0,1]
	v_cvt_scalef32_pk_f32_fp4 v[224:225], v184, 1.0 op_sel:[0,1,0]
	v_pk_fma_f32 v[62:63], v[224:225], v[216:217], v[62:63] op_sel_hi:[1,0,1]
	v_cvt_scalef32_pk_f32_fp4 v[226:227], v184, 1.0 op_sel:[1,1,0]
	v_pk_fma_f32 v[60:61], v[226:227], v[216:217], v[60:61] op_sel_hi:[1,0,1]
	v_cvt_scalef32_pk_f32_fp4 v[220:221], v185, 1.0
	v_pk_fma_f32 v[58:59], v[220:221], v[216:217], v[58:59] op_sel_hi:[1,0,1]
	v_cvt_scalef32_pk_f32_fp4 v[222:223], v185, 1.0 op_sel:[1,0,0]
	v_pk_fma_f32 v[56:57], v[222:223], v[216:217], v[56:57] op_sel_hi:[1,0,1]
	v_cvt_scalef32_pk_f32_fp4 v[224:225], v185, 1.0 op_sel:[0,1,0]
	v_pk_fma_f32 v[54:55], v[224:225], v[216:217], v[54:55] op_sel_hi:[1,0,1]
	v_cvt_scalef32_pk_f32_fp4 v[226:227], v185, 1.0 op_sel:[1,1,0]
	v_pk_fma_f32 v[52:53], v[226:227], v[216:217], v[52:53] op_sel_hi:[1,0,1]
	v_cvt_scalef32_pk_f32_fp4 v[220:221], v186, 1.0
	v_pk_fma_f32 v[50:51], v[220:221], v[216:217], v[50:51] op_sel_hi:[1,0,1]
	v_cvt_scalef32_pk_f32_fp4 v[222:223], v186, 1.0 op_sel:[1,0,0]
	v_pk_fma_f32 v[46:47], v[222:223], v[216:217], v[46:47] op_sel_hi:[1,0,1]
	v_cvt_scalef32_pk_f32_fp4 v[224:225], v186, 1.0 op_sel:[0,1,0]
	v_pk_fma_f32 v[44:45], v[224:225], v[216:217], v[44:45] op_sel_hi:[1,0,1]
	v_cvt_scalef32_pk_f32_fp4 v[226:227], v186, 1.0 op_sel:[1,1,0]
	v_pk_fma_f32 v[42:43], v[226:227], v[216:217], v[42:43] op_sel_hi:[1,0,1]
	v_cvt_scalef32_pk_f32_fp4 v[220:221], v187, 1.0
	v_pk_fma_f32 v[40:41], v[220:221], v[216:217], v[40:41] op_sel_hi:[1,0,1]
	v_cvt_scalef32_pk_f32_fp4 v[222:223], v187, 1.0 op_sel:[1,0,0]
	v_pk_fma_f32 v[38:39], v[222:223], v[216:217], v[38:39] op_sel_hi:[1,0,1]
	v_cvt_scalef32_pk_f32_fp4 v[224:225], v187, 1.0 op_sel:[0,1,0]
	v_pk_fma_f32 v[36:37], v[224:225], v[216:217], v[36:37] op_sel_hi:[1,0,1]
	v_cvt_scalef32_pk_f32_fp4 v[226:227], v187, 1.0 op_sel:[1,1,0]
	v_pk_fma_f32 v[34:35], v[226:227], v[216:217], v[34:35] op_sel_hi:[1,0,1]
	s_waitcnt vmcnt(4)
	v_cvt_scalef32_pk_f32_fp4 v[220:221], v188, 1.0
	v_pk_fma_f32 v[96:97], v[220:221], v[216:217], v[96:97] op_sel:[0,1,0] op_sel_hi:[1,1,1]
	v_cvt_scalef32_pk_f32_fp4 v[222:223], v188, 1.0 op_sel:[1,0,0]
	v_pk_fma_f32 v[98:99], v[222:223], v[216:217], v[98:99] op_sel:[0,1,0] op_sel_hi:[1,1,1]
	v_cvt_scalef32_pk_f32_fp4 v[224:225], v188, 1.0 op_sel:[0,1,0]
	v_pk_fma_f32 v[94:95], v[224:225], v[216:217], v[94:95] op_sel:[0,1,0] op_sel_hi:[1,1,1]
	v_cvt_scalef32_pk_f32_fp4 v[226:227], v188, 1.0 op_sel:[1,1,0]
	v_pk_fma_f32 v[92:93], v[226:227], v[216:217], v[92:93] op_sel:[0,1,0] op_sel_hi:[1,1,1]
	v_cvt_scalef32_pk_f32_fp4 v[220:221], v189, 1.0
	v_pk_fma_f32 v[90:91], v[220:221], v[216:217], v[90:91] op_sel:[0,1,0] op_sel_hi:[1,1,1]
	v_cvt_scalef32_pk_f32_fp4 v[222:223], v189, 1.0 op_sel:[1,0,0]
	v_pk_fma_f32 v[88:89], v[222:223], v[216:217], v[88:89] op_sel:[0,1,0] op_sel_hi:[1,1,1]
	v_cvt_scalef32_pk_f32_fp4 v[224:225], v189, 1.0 op_sel:[0,1,0]
	v_pk_fma_f32 v[86:87], v[224:225], v[216:217], v[86:87] op_sel:[0,1,0] op_sel_hi:[1,1,1]
	v_cvt_scalef32_pk_f32_fp4 v[226:227], v189, 1.0 op_sel:[1,1,0]
	v_pk_fma_f32 v[84:85], v[226:227], v[216:217], v[84:85] op_sel:[0,1,0] op_sel_hi:[1,1,1]
	v_cvt_scalef32_pk_f32_fp4 v[220:221], v190, 1.0
	v_pk_fma_f32 v[82:83], v[220:221], v[216:217], v[82:83] op_sel:[0,1,0] op_sel_hi:[1,1,1]
	v_cvt_scalef32_pk_f32_fp4 v[222:223], v190, 1.0 op_sel:[1,0,0]
	v_pk_fma_f32 v[80:81], v[222:223], v[216:217], v[80:81] op_sel:[0,1,0] op_sel_hi:[1,1,1]
	v_cvt_scalef32_pk_f32_fp4 v[224:225], v190, 1.0 op_sel:[0,1,0]
	v_pk_fma_f32 v[78:79], v[224:225], v[216:217], v[78:79] op_sel:[0,1,0] op_sel_hi:[1,1,1]
	v_cvt_scalef32_pk_f32_fp4 v[226:227], v190, 1.0 op_sel:[1,1,0]
	v_pk_fma_f32 v[76:77], v[226:227], v[216:217], v[76:77] op_sel:[0,1,0] op_sel_hi:[1,1,1]
	v_cvt_scalef32_pk_f32_fp4 v[220:221], v191, 1.0
	v_pk_fma_f32 v[74:75], v[220:221], v[216:217], v[74:75] op_sel:[0,1,0] op_sel_hi:[1,1,1]
	v_cvt_scalef32_pk_f32_fp4 v[222:223], v191, 1.0 op_sel:[1,0,0]
	v_pk_fma_f32 v[72:73], v[222:223], v[216:217], v[72:73] op_sel:[0,1,0] op_sel_hi:[1,1,1]
	v_cvt_scalef32_pk_f32_fp4 v[224:225], v191, 1.0 op_sel:[0,1,0]
	v_pk_fma_f32 v[70:71], v[224:225], v[216:217], v[70:71] op_sel:[0,1,0] op_sel_hi:[1,1,1]
	v_cvt_scalef32_pk_f32_fp4 v[226:227], v191, 1.0 op_sel:[1,1,0]
	v_pk_fma_f32 v[68:69], v[226:227], v[216:217], v[68:69] op_sel:[0,1,0] op_sel_hi:[1,1,1]
	v_cvt_scalef32_pk_f32_fp4 v[220:221], v192, 1.0
	v_pk_fma_f32 v[66:67], v[220:221], v[216:217], v[66:67] op_sel:[0,1,0] op_sel_hi:[1,1,1]
	v_cvt_scalef32_pk_f32_fp4 v[222:223], v192, 1.0 op_sel:[1,0,0]
	v_pk_fma_f32 v[64:65], v[222:223], v[216:217], v[64:65] op_sel:[0,1,0] op_sel_hi:[1,1,1]
	v_cvt_scalef32_pk_f32_fp4 v[224:225], v192, 1.0 op_sel:[0,1,0]
	v_pk_fma_f32 v[62:63], v[224:225], v[216:217], v[62:63] op_sel:[0,1,0] op_sel_hi:[1,1,1]
	v_cvt_scalef32_pk_f32_fp4 v[226:227], v192, 1.0 op_sel:[1,1,0]
	v_pk_fma_f32 v[60:61], v[226:227], v[216:217], v[60:61] op_sel:[0,1,0] op_sel_hi:[1,1,1]
	v_cvt_scalef32_pk_f32_fp4 v[220:221], v193, 1.0
	v_pk_fma_f32 v[58:59], v[220:221], v[216:217], v[58:59] op_sel:[0,1,0] op_sel_hi:[1,1,1]
	v_cvt_scalef32_pk_f32_fp4 v[222:223], v193, 1.0 op_sel:[1,0,0]
	v_pk_fma_f32 v[56:57], v[222:223], v[216:217], v[56:57] op_sel:[0,1,0] op_sel_hi:[1,1,1]
	v_cvt_scalef32_pk_f32_fp4 v[224:225], v193, 1.0 op_sel:[0,1,0]
	v_pk_fma_f32 v[54:55], v[224:225], v[216:217], v[54:55] op_sel:[0,1,0] op_sel_hi:[1,1,1]
	v_cvt_scalef32_pk_f32_fp4 v[226:227], v193, 1.0 op_sel:[1,1,0]
	v_pk_fma_f32 v[52:53], v[226:227], v[216:217], v[52:53] op_sel:[0,1,0] op_sel_hi:[1,1,1]
	v_cvt_scalef32_pk_f32_fp4 v[220:221], v194, 1.0
	v_pk_fma_f32 v[50:51], v[220:221], v[216:217], v[50:51] op_sel:[0,1,0] op_sel_hi:[1,1,1]
	v_cvt_scalef32_pk_f32_fp4 v[222:223], v194, 1.0 op_sel:[1,0,0]
	v_pk_fma_f32 v[46:47], v[222:223], v[216:217], v[46:47] op_sel:[0,1,0] op_sel_hi:[1,1,1]
	v_cvt_scalef32_pk_f32_fp4 v[224:225], v194, 1.0 op_sel:[0,1,0]
	v_pk_fma_f32 v[44:45], v[224:225], v[216:217], v[44:45] op_sel:[0,1,0] op_sel_hi:[1,1,1]
	v_cvt_scalef32_pk_f32_fp4 v[226:227], v194, 1.0 op_sel:[1,1,0]
	v_pk_fma_f32 v[42:43], v[226:227], v[216:217], v[42:43] op_sel:[0,1,0] op_sel_hi:[1,1,1]
	v_cvt_scalef32_pk_f32_fp4 v[220:221], v195, 1.0
	v_pk_fma_f32 v[40:41], v[220:221], v[216:217], v[40:41] op_sel:[0,1,0] op_sel_hi:[1,1,1]
	v_cvt_scalef32_pk_f32_fp4 v[222:223], v195, 1.0 op_sel:[1,0,0]
	v_pk_fma_f32 v[38:39], v[222:223], v[216:217], v[38:39] op_sel:[0,1,0] op_sel_hi:[1,1,1]
	v_cvt_scalef32_pk_f32_fp4 v[224:225], v195, 1.0 op_sel:[0,1,0]
	v_pk_fma_f32 v[36:37], v[224:225], v[216:217], v[36:37] op_sel:[0,1,0] op_sel_hi:[1,1,1]
	v_cvt_scalef32_pk_f32_fp4 v[226:227], v195, 1.0 op_sel:[1,1,0]
	v_pk_fma_f32 v[34:35], v[226:227], v[216:217], v[34:35] op_sel:[0,1,0] op_sel_hi:[1,1,1]
	s_waitcnt vmcnt(2)
	v_cvt_scalef32_pk_f32_fp4 v[220:221], v196, 1.0
	v_pk_fma_f32 v[96:97], v[220:221], v[218:219], v[96:97] op_sel_hi:[1,0,1]
	v_cvt_scalef32_pk_f32_fp4 v[222:223], v196, 1.0 op_sel:[1,0,0]
	v_pk_fma_f32 v[98:99], v[222:223], v[218:219], v[98:99] op_sel_hi:[1,0,1]
	v_cvt_scalef32_pk_f32_fp4 v[224:225], v196, 1.0 op_sel:[0,1,0]
	v_pk_fma_f32 v[94:95], v[224:225], v[218:219], v[94:95] op_sel_hi:[1,0,1]
	v_cvt_scalef32_pk_f32_fp4 v[226:227], v196, 1.0 op_sel:[1,1,0]
	v_pk_fma_f32 v[92:93], v[226:227], v[218:219], v[92:93] op_sel_hi:[1,0,1]
	v_cvt_scalef32_pk_f32_fp4 v[220:221], v197, 1.0
	v_pk_fma_f32 v[90:91], v[220:221], v[218:219], v[90:91] op_sel_hi:[1,0,1]
	v_cvt_scalef32_pk_f32_fp4 v[222:223], v197, 1.0 op_sel:[1,0,0]
	v_pk_fma_f32 v[88:89], v[222:223], v[218:219], v[88:89] op_sel_hi:[1,0,1]
	v_cvt_scalef32_pk_f32_fp4 v[224:225], v197, 1.0 op_sel:[0,1,0]
	v_pk_fma_f32 v[86:87], v[224:225], v[218:219], v[86:87] op_sel_hi:[1,0,1]
	v_cvt_scalef32_pk_f32_fp4 v[226:227], v197, 1.0 op_sel:[1,1,0]
	v_pk_fma_f32 v[84:85], v[226:227], v[218:219], v[84:85] op_sel_hi:[1,0,1]
	v_cvt_scalef32_pk_f32_fp4 v[220:221], v198, 1.0
	v_pk_fma_f32 v[82:83], v[220:221], v[218:219], v[82:83] op_sel_hi:[1,0,1]
	v_cvt_scalef32_pk_f32_fp4 v[222:223], v198, 1.0 op_sel:[1,0,0]
	v_pk_fma_f32 v[80:81], v[222:223], v[218:219], v[80:81] op_sel_hi:[1,0,1]
	v_cvt_scalef32_pk_f32_fp4 v[224:225], v198, 1.0 op_sel:[0,1,0]
	v_pk_fma_f32 v[78:79], v[224:225], v[218:219], v[78:79] op_sel_hi:[1,0,1]
	v_cvt_scalef32_pk_f32_fp4 v[226:227], v198, 1.0 op_sel:[1,1,0]
	v_pk_fma_f32 v[76:77], v[226:227], v[218:219], v[76:77] op_sel_hi:[1,0,1]
	v_cvt_scalef32_pk_f32_fp4 v[220:221], v199, 1.0
	v_pk_fma_f32 v[74:75], v[220:221], v[218:219], v[74:75] op_sel_hi:[1,0,1]
	v_cvt_scalef32_pk_f32_fp4 v[222:223], v199, 1.0 op_sel:[1,0,0]
	v_pk_fma_f32 v[72:73], v[222:223], v[218:219], v[72:73] op_sel_hi:[1,0,1]
	v_cvt_scalef32_pk_f32_fp4 v[224:225], v199, 1.0 op_sel:[0,1,0]
	v_pk_fma_f32 v[70:71], v[224:225], v[218:219], v[70:71] op_sel_hi:[1,0,1]
	v_cvt_scalef32_pk_f32_fp4 v[226:227], v199, 1.0 op_sel:[1,1,0]
	v_pk_fma_f32 v[68:69], v[226:227], v[218:219], v[68:69] op_sel_hi:[1,0,1]
	v_cvt_scalef32_pk_f32_fp4 v[220:221], v200, 1.0
	v_pk_fma_f32 v[66:67], v[220:221], v[218:219], v[66:67] op_sel_hi:[1,0,1]
	v_cvt_scalef32_pk_f32_fp4 v[222:223], v200, 1.0 op_sel:[1,0,0]
	v_pk_fma_f32 v[64:65], v[222:223], v[218:219], v[64:65] op_sel_hi:[1,0,1]
	v_cvt_scalef32_pk_f32_fp4 v[224:225], v200, 1.0 op_sel:[0,1,0]
	v_pk_fma_f32 v[62:63], v[224:225], v[218:219], v[62:63] op_sel_hi:[1,0,1]
	v_cvt_scalef32_pk_f32_fp4 v[226:227], v200, 1.0 op_sel:[1,1,0]
	v_pk_fma_f32 v[60:61], v[226:227], v[218:219], v[60:61] op_sel_hi:[1,0,1]
	v_cvt_scalef32_pk_f32_fp4 v[220:221], v201, 1.0
	v_pk_fma_f32 v[58:59], v[220:221], v[218:219], v[58:59] op_sel_hi:[1,0,1]
	v_cvt_scalef32_pk_f32_fp4 v[222:223], v201, 1.0 op_sel:[1,0,0]
	v_pk_fma_f32 v[56:57], v[222:223], v[218:219], v[56:57] op_sel_hi:[1,0,1]
	v_cvt_scalef32_pk_f32_fp4 v[224:225], v201, 1.0 op_sel:[0,1,0]
	v_pk_fma_f32 v[54:55], v[224:225], v[218:219], v[54:55] op_sel_hi:[1,0,1]
	v_cvt_scalef32_pk_f32_fp4 v[226:227], v201, 1.0 op_sel:[1,1,0]
	v_pk_fma_f32 v[52:53], v[226:227], v[218:219], v[52:53] op_sel_hi:[1,0,1]
	v_cvt_scalef32_pk_f32_fp4 v[220:221], v202, 1.0
	v_pk_fma_f32 v[50:51], v[220:221], v[218:219], v[50:51] op_sel_hi:[1,0,1]
	v_cvt_scalef32_pk_f32_fp4 v[222:223], v202, 1.0 op_sel:[1,0,0]
	v_pk_fma_f32 v[46:47], v[222:223], v[218:219], v[46:47] op_sel_hi:[1,0,1]
	v_cvt_scalef32_pk_f32_fp4 v[224:225], v202, 1.0 op_sel:[0,1,0]
	v_pk_fma_f32 v[44:45], v[224:225], v[218:219], v[44:45] op_sel_hi:[1,0,1]
	v_cvt_scalef32_pk_f32_fp4 v[226:227], v202, 1.0 op_sel:[1,1,0]
	v_pk_fma_f32 v[42:43], v[226:227], v[218:219], v[42:43] op_sel_hi:[1,0,1]
	v_cvt_scalef32_pk_f32_fp4 v[220:221], v203, 1.0
	v_pk_fma_f32 v[40:41], v[220:221], v[218:219], v[40:41] op_sel_hi:[1,0,1]
	v_cvt_scalef32_pk_f32_fp4 v[222:223], v203, 1.0 op_sel:[1,0,0]
	v_pk_fma_f32 v[38:39], v[222:223], v[218:219], v[38:39] op_sel_hi:[1,0,1]
	v_cvt_scalef32_pk_f32_fp4 v[224:225], v203, 1.0 op_sel:[0,1,0]
	v_pk_fma_f32 v[36:37], v[224:225], v[218:219], v[36:37] op_sel_hi:[1,0,1]
	v_cvt_scalef32_pk_f32_fp4 v[226:227], v203, 1.0 op_sel:[1,1,0]
	v_pk_fma_f32 v[34:35], v[226:227], v[218:219], v[34:35] op_sel_hi:[1,0,1]
	s_waitcnt vmcnt(0)
	v_cvt_scalef32_pk_f32_fp4 v[220:221], v204, 1.0
	v_pk_fma_f32 v[96:97], v[220:221], v[218:219], v[96:97] op_sel:[0,1,0] op_sel_hi:[1,1,1]
	v_cvt_scalef32_pk_f32_fp4 v[222:223], v204, 1.0 op_sel:[1,0,0]
	v_pk_fma_f32 v[98:99], v[222:223], v[218:219], v[98:99] op_sel:[0,1,0] op_sel_hi:[1,1,1]
	v_cvt_scalef32_pk_f32_fp4 v[224:225], v204, 1.0 op_sel:[0,1,0]
	v_pk_fma_f32 v[94:95], v[224:225], v[218:219], v[94:95] op_sel:[0,1,0] op_sel_hi:[1,1,1]
	v_cvt_scalef32_pk_f32_fp4 v[226:227], v204, 1.0 op_sel:[1,1,0]
	v_pk_fma_f32 v[92:93], v[226:227], v[218:219], v[92:93] op_sel:[0,1,0] op_sel_hi:[1,1,1]
	v_cvt_scalef32_pk_f32_fp4 v[220:221], v205, 1.0
	v_pk_fma_f32 v[90:91], v[220:221], v[218:219], v[90:91] op_sel:[0,1,0] op_sel_hi:[1,1,1]
	v_cvt_scalef32_pk_f32_fp4 v[222:223], v205, 1.0 op_sel:[1,0,0]
	v_pk_fma_f32 v[88:89], v[222:223], v[218:219], v[88:89] op_sel:[0,1,0] op_sel_hi:[1,1,1]
	v_cvt_scalef32_pk_f32_fp4 v[224:225], v205, 1.0 op_sel:[0,1,0]
	v_pk_fma_f32 v[86:87], v[224:225], v[218:219], v[86:87] op_sel:[0,1,0] op_sel_hi:[1,1,1]
	v_cvt_scalef32_pk_f32_fp4 v[226:227], v205, 1.0 op_sel:[1,1,0]
	v_pk_fma_f32 v[84:85], v[226:227], v[218:219], v[84:85] op_sel:[0,1,0] op_sel_hi:[1,1,1]
	v_cvt_scalef32_pk_f32_fp4 v[220:221], v206, 1.0
	v_pk_fma_f32 v[82:83], v[220:221], v[218:219], v[82:83] op_sel:[0,1,0] op_sel_hi:[1,1,1]
	v_cvt_scalef32_pk_f32_fp4 v[222:223], v206, 1.0 op_sel:[1,0,0]
	v_pk_fma_f32 v[80:81], v[222:223], v[218:219], v[80:81] op_sel:[0,1,0] op_sel_hi:[1,1,1]
	v_cvt_scalef32_pk_f32_fp4 v[224:225], v206, 1.0 op_sel:[0,1,0]
	v_pk_fma_f32 v[78:79], v[224:225], v[218:219], v[78:79] op_sel:[0,1,0] op_sel_hi:[1,1,1]
	v_cvt_scalef32_pk_f32_fp4 v[226:227], v206, 1.0 op_sel:[1,1,0]
	v_pk_fma_f32 v[76:77], v[226:227], v[218:219], v[76:77] op_sel:[0,1,0] op_sel_hi:[1,1,1]
	v_cvt_scalef32_pk_f32_fp4 v[220:221], v207, 1.0
	v_pk_fma_f32 v[74:75], v[220:221], v[218:219], v[74:75] op_sel:[0,1,0] op_sel_hi:[1,1,1]
	v_cvt_scalef32_pk_f32_fp4 v[222:223], v207, 1.0 op_sel:[1,0,0]
	v_pk_fma_f32 v[72:73], v[222:223], v[218:219], v[72:73] op_sel:[0,1,0] op_sel_hi:[1,1,1]
	v_cvt_scalef32_pk_f32_fp4 v[224:225], v207, 1.0 op_sel:[0,1,0]
	v_pk_fma_f32 v[70:71], v[224:225], v[218:219], v[70:71] op_sel:[0,1,0] op_sel_hi:[1,1,1]
	v_cvt_scalef32_pk_f32_fp4 v[226:227], v207, 1.0 op_sel:[1,1,0]
	v_pk_fma_f32 v[68:69], v[226:227], v[218:219], v[68:69] op_sel:[0,1,0] op_sel_hi:[1,1,1]
	v_cvt_scalef32_pk_f32_fp4 v[220:221], v208, 1.0
	v_pk_fma_f32 v[66:67], v[220:221], v[218:219], v[66:67] op_sel:[0,1,0] op_sel_hi:[1,1,1]
	v_cvt_scalef32_pk_f32_fp4 v[222:223], v208, 1.0 op_sel:[1,0,0]
	v_pk_fma_f32 v[64:65], v[222:223], v[218:219], v[64:65] op_sel:[0,1,0] op_sel_hi:[1,1,1]
	v_cvt_scalef32_pk_f32_fp4 v[224:225], v208, 1.0 op_sel:[0,1,0]
	v_pk_fma_f32 v[62:63], v[224:225], v[218:219], v[62:63] op_sel:[0,1,0] op_sel_hi:[1,1,1]
	v_cvt_scalef32_pk_f32_fp4 v[226:227], v208, 1.0 op_sel:[1,1,0]
	v_pk_fma_f32 v[60:61], v[226:227], v[218:219], v[60:61] op_sel:[0,1,0] op_sel_hi:[1,1,1]
	v_cvt_scalef32_pk_f32_fp4 v[220:221], v209, 1.0
	v_pk_fma_f32 v[58:59], v[220:221], v[218:219], v[58:59] op_sel:[0,1,0] op_sel_hi:[1,1,1]
	v_cvt_scalef32_pk_f32_fp4 v[222:223], v209, 1.0 op_sel:[1,0,0]
	v_pk_fma_f32 v[56:57], v[222:223], v[218:219], v[56:57] op_sel:[0,1,0] op_sel_hi:[1,1,1]
	v_cvt_scalef32_pk_f32_fp4 v[224:225], v209, 1.0 op_sel:[0,1,0]
	v_pk_fma_f32 v[54:55], v[224:225], v[218:219], v[54:55] op_sel:[0,1,0] op_sel_hi:[1,1,1]
	v_cvt_scalef32_pk_f32_fp4 v[226:227], v209, 1.0 op_sel:[1,1,0]
	v_pk_fma_f32 v[52:53], v[226:227], v[218:219], v[52:53] op_sel:[0,1,0] op_sel_hi:[1,1,1]
	v_cvt_scalef32_pk_f32_fp4 v[220:221], v210, 1.0
	v_pk_fma_f32 v[50:51], v[220:221], v[218:219], v[50:51] op_sel:[0,1,0] op_sel_hi:[1,1,1]
	v_cvt_scalef32_pk_f32_fp4 v[222:223], v210, 1.0 op_sel:[1,0,0]
	v_pk_fma_f32 v[46:47], v[222:223], v[218:219], v[46:47] op_sel:[0,1,0] op_sel_hi:[1,1,1]
	v_cvt_scalef32_pk_f32_fp4 v[224:225], v210, 1.0 op_sel:[0,1,0]
	v_pk_fma_f32 v[44:45], v[224:225], v[218:219], v[44:45] op_sel:[0,1,0] op_sel_hi:[1,1,1]
	v_cvt_scalef32_pk_f32_fp4 v[226:227], v210, 1.0 op_sel:[1,1,0]
	v_pk_fma_f32 v[42:43], v[226:227], v[218:219], v[42:43] op_sel:[0,1,0] op_sel_hi:[1,1,1]
	v_cvt_scalef32_pk_f32_fp4 v[220:221], v211, 1.0
	v_pk_fma_f32 v[40:41], v[220:221], v[218:219], v[40:41] op_sel:[0,1,0] op_sel_hi:[1,1,1]
	v_cvt_scalef32_pk_f32_fp4 v[222:223], v211, 1.0 op_sel:[1,0,0]
	v_pk_fma_f32 v[38:39], v[222:223], v[218:219], v[38:39] op_sel:[0,1,0] op_sel_hi:[1,1,1]
	v_cvt_scalef32_pk_f32_fp4 v[224:225], v211, 1.0 op_sel:[0,1,0]
	v_pk_fma_f32 v[36:37], v[224:225], v[218:219], v[36:37] op_sel:[0,1,0] op_sel_hi:[1,1,1]
	v_cvt_scalef32_pk_f32_fp4 v[226:227], v211, 1.0 op_sel:[1,1,0]
	v_pk_fma_f32 v[34:35], v[226:227], v[218:219], v[34:35] op_sel:[0,1,0] op_sel_hi:[1,1,1]
	s_add_i32 s0, s9, s8
	v_mov_b32_e32 v48, v145
	s_ashr_i32 s1, s0, 31
	s_lshl_b64 s[10:11], s[0:1], 13
	s_waitcnt vmcnt(1)
	v_lshlrev_b32_e32 v22, 2, v48
	s_add_u32 s10, s28, s10
	v_add_u32_e32 v24, 0x800, v22
	v_add_u32_e32 v26, 0x900, v22
	s_addc_u32 s11, s29, s11
	v_ashrrev_i32_e32 v23, 31, v22
	v_ashrrev_i32_e32 v25, 31, v24
	v_ashrrev_i32_e32 v27, 31, v26
	v_lshl_add_u64 v[0:1], v[22:23], 1, s[10:11]
	v_lshl_add_u64 v[16:17], v[24:25], 1, s[10:11]
	v_lshl_add_u64 v[18:19], v[26:27], 1, s[10:11]
	global_load_dwordx2 v[2:3], v[0:1], off
	global_load_dwordx2 v[4:5], v[0:1], off offset:512
	global_load_dwordx2 v[6:7], v[0:1], off offset:1024
	global_load_dwordx2 v[8:9], v[0:1], off offset:1536
	global_load_dwordx2 v[10:11], v[0:1], off offset:2048
	global_load_dwordx2 v[12:13], v[0:1], off offset:2560
	global_load_dwordx2 v[14:15], v[0:1], off offset:3072
	s_nop 0
	global_load_dwordx2 v[0:1], v[0:1], off offset:3584
	v_add_u32_e32 v28, 0xa00, v22
	global_load_dwordx2 v[16:17], v[16:17], off
	v_ashrrev_i32_e32 v29, 31, v28
	global_load_dwordx2 v[18:19], v[18:19], off
	v_add_u32_e32 v30, 0xb00, v22
	v_lshl_add_u64 v[20:21], v[28:29], 1, s[10:11]
	v_ashrrev_i32_e32 v31, 31, v30
	v_add_u32_e32 v102, 0xc00, v22
	global_load_dwordx2 v[112:113], v[20:21], off
	v_lshl_add_u64 v[20:21], v[30:31], 1, s[10:11]
	v_ashrrev_i32_e32 v103, 31, v102
	v_add_u32_e32 v100, 0xd00, v22
	global_load_dwordx2 v[114:115], v[20:21], off
	v_lshl_add_u64 v[20:21], v[102:103], 1, s[10:11]
	v_ashrrev_i32_e32 v101, 31, v100
	v_add_u32_e32 v104, 0xe00, v22
	global_load_dwordx2 v[116:117], v[20:21], off
	v_lshl_add_u64 v[20:21], v[100:101], 1, s[10:11]
	v_ashrrev_i32_e32 v105, 31, v104
	global_load_dwordx2 v[118:119], v[20:21], off
	v_lshl_add_u64 v[20:21], v[104:105], 1, s[10:11]
	global_load_dwordx2 v[192:193], v[20:21], off
	v_add_u32_e32 v20, 0xf00, v22
	v_ashrrev_i32_e32 v21, 31, v20
	v_lshl_add_u64 v[110:111], v[20:21], 1, s[10:11]
	global_load_dwordx2 v[194:195], v[110:111], off
	v_lshl_add_u32 v48, v48, 4, 0
	v_add_u32_e32 v147, 0x10100, v48
	ds_read_b128 v[148:151], v147
	ds_read_b128 v[152:155], v147 offset:1024
	ds_read_b128 v[156:159], v147 offset:2048
	ds_read_b128 v[160:163], v147 offset:3072
	ds_read_b128 v[164:167], v147 offset:4096
	ds_read_b128 v[168:171], v147 offset:5120
	ds_read_b128 v[172:175], v147 offset:6144
	ds_read_b128 v[176:179], v147 offset:7168
	ds_read_b128 v[180:183], v147 offset:8192
	ds_read_b128 v[184:187], v147 offset:9216
	s_lshl_b64 s[0:1], s[0:1], 14
	s_add_u32 s10, s52, s0
	s_addc_u32 s11, s53, s1
	v_add_u32_e32 v108, 0x400, v22
	v_add_u32_e32 v106, 0x500, v22
	v_add_u32_e32 v110, 0x600, v22
	v_ashrrev_i32_e32 v109, 31, v108
	v_ashrrev_i32_e32 v107, 31, v106
	v_lshl_add_u64 v[30:31], v[30:31], 2, s[10:11]
	v_lshl_add_u64 v[100:101], v[100:101], 2, s[10:11]
	s_mov_b32 s9, 1
	v_lshl_add_u64 v[102:103], v[102:103], 2, s[10:11]
	v_lshl_add_u64 v[104:105], v[104:105], 2, s[10:11]
	s_waitcnt vmcnt(15)
	v_lshlrev_b32_e32 v196, 16, v2
	v_and_b32_e32 v197, 0xffff0000, v2
	s_waitcnt vmcnt(14)
	v_lshlrev_b32_e32 v200, 16, v4
	v_and_b32_e32 v201, 0xffff0000, v4
	v_lshlrev_b32_e32 v198, 16, v3
	v_and_b32_e32 v199, 0xffff0000, v3
	v_lshlrev_b32_e32 v202, 16, v5
	v_and_b32_e32 v203, 0xffff0000, v5
	s_waitcnt vmcnt(13)
	v_lshlrev_b32_e32 v204, 16, v6
	v_and_b32_e32 v205, 0xffff0000, v6
	v_lshlrev_b32_e32 v206, 16, v7
	v_and_b32_e32 v207, 0xffff0000, v7
	s_waitcnt vmcnt(12)
	v_lshlrev_b32_e32 v208, 16, v8
	v_and_b32_e32 v209, 0xffff0000, v8
	v_lshlrev_b32_e32 v210, 16, v9
	v_and_b32_e32 v211, 0xffff0000, v9
	s_waitcnt vmcnt(11)
	v_lshlrev_b32_e32 v212, 16, v10
	v_and_b32_e32 v213, 0xffff0000, v10
	v_lshlrev_b32_e32 v214, 16, v11
	v_and_b32_e32 v215, 0xffff0000, v11
	s_waitcnt vmcnt(10)
	v_lshlrev_b32_e32 v216, 16, v12
	v_and_b32_e32 v217, 0xffff0000, v12
	v_lshlrev_b32_e32 v218, 16, v13
	v_and_b32_e32 v219, 0xffff0000, v13
	s_waitcnt vmcnt(9)
	v_lshlrev_b32_e32 v220, 16, v14
	v_and_b32_e32 v221, 0xffff0000, v14
	v_lshlrev_b32_e32 v222, 16, v15
	v_and_b32_e32 v223, 0xffff0000, v15
	s_waitcnt vmcnt(8)
	v_lshlrev_b32_e32 v224, 16, v0
	v_and_b32_e32 v225, 0xffff0000, v0
	v_lshlrev_b32_e32 v226, 16, v1
	v_and_b32_e32 v227, 0xffff0000, v1
	s_waitcnt vmcnt(7)
	v_lshlrev_b32_e32 v228, 16, v16
	v_and_b32_e32 v229, 0xffff0000, v16
	v_lshlrev_b32_e32 v230, 16, v17
	v_and_b32_e32 v231, 0xffff0000, v17
	s_waitcnt vmcnt(6)
	v_lshlrev_b32_e32 v232, 16, v18
	v_and_b32_e32 v233, 0xffff0000, v18
	v_lshlrev_b32_e32 v234, 16, v19
	v_and_b32_e32 v235, 0xffff0000, v19
	ds_read_b128 v[188:191], v147 offset:10240
	ds_read_b128 v[16:19], v147 offset:11264
	ds_read_b128 v[12:15], v147 offset:12288
	ds_read_b128 v[8:11], v147 offset:13312
	ds_read_b128 v[4:7], v147 offset:14336
	ds_read_b128 v[0:3], v147 offset:15360
	s_waitcnt lgkmcnt(14)
	v_pk_fma_f32 v[96:97], v[96:97], v[148:149], v[196:197]
	v_pk_fma_f32 v[94:95], v[94:95], v[152:153], v[200:201]
	v_pk_fma_f32 v[98:99], v[98:99], v[150:151], v[198:199]
	v_pk_fma_f32 v[92:93], v[92:93], v[154:155], v[202:203]
	v_mov_b32_e32 v150, v97
	v_mov_b32_e32 v151, v95
	v_mov_b32_e32 v148, v96
	v_mov_b32_e32 v149, v94
	v_pk_mul_f32 v[150:151], v[150:151], v[150:151]
	v_mov_b32_e32 v152, v99
	v_mov_b32_e32 v153, v93
	v_pk_fma_f32 v[148:149], v[148:149], v[148:149], v[150:151]
	v_mov_b32_e32 v150, v98
	v_mov_b32_e32 v151, v92
	v_pk_mul_f32 v[152:153], v[152:153], v[152:153]
	s_waitcnt lgkmcnt(13)
	v_pk_fma_f32 v[90:91], v[90:91], v[156:157], v[204:205]
	v_pk_fma_f32 v[88:89], v[88:89], v[158:159], v[206:207]
	v_pk_fma_f32 v[150:151], v[150:151], v[150:151], v[152:153]
	v_mov_b32_e32 v152, v91
	v_mov_b32_e32 v153, v89
	s_waitcnt lgkmcnt(12)
	v_pk_fma_f32 v[86:87], v[86:87], v[160:161], v[208:209]
	s_waitcnt lgkmcnt(0)
	v_mul_f32_e32 v36, v36, v0
	v_pk_add_f32 v[148:149], v[148:149], v[150:151]
	v_mov_b32_e32 v150, v90
	v_mov_b32_e32 v151, v88
	v_pk_mul_f32 v[152:153], v[152:153], v[152:153]
	v_mul_f32_e32 v0, v87, v87
	v_pk_fma_f32 v[84:85], v[84:85], v[162:163], v[210:211]
	v_pk_fma_f32 v[150:151], v[150:151], v[150:151], v[152:153]
	v_pk_fma_f32 v[152:153], v[86:87], v[86:87], v[0:1] op_sel_hi:[1,1,0]
	v_mul_f32_e32 v0, v85, v85
	v_pk_fma_f32 v[82:83], v[82:83], v[164:165], v[212:213]
	v_pk_fma_f32 v[80:81], v[80:81], v[166:167], v[214:215]
	v_pk_add_f32 v[148:149], v[148:149], v[148:149] op_sel:[0,1] op_sel_hi:[1,0]
	v_pk_add_f32 v[150:151], v[150:151], v[150:151] op_sel:[0,1] op_sel_hi:[1,0]
	v_pk_fma_f32 v[154:155], v[84:85], v[84:85], v[0:1] op_sel_hi:[1,1,0]
	v_pk_mul_f32 v[156:157], v[82:83], v[82:83]
	v_pk_mul_f32 v[158:159], v[80:81], v[80:81]
	v_mov_b32_e32 v149, v156
	v_mov_b32_e32 v151, v157
	v_mov_b32_e32 v153, v158
	v_mov_b32_e32 v155, v159
	v_pk_fma_f32 v[78:79], v[78:79], v[168:169], v[216:217]
	v_pk_fma_f32 v[76:77], v[76:77], v[170:171], v[218:219]
	v_pk_add_f32 v[148:149], v[148:149], v[150:151]
	v_pk_add_f32 v[150:151], v[152:153], v[154:155]
	v_mov_b32_e32 v152, v79
	v_mov_b32_e32 v153, v77
	v_pk_fma_f32 v[74:75], v[74:75], v[172:173], v[220:221]
	v_pk_add_f32 v[148:149], v[148:149], v[150:151]
	v_mov_b32_e32 v150, v78
	v_mov_b32_e32 v151, v76
	v_pk_mul_f32 v[152:153], v[152:153], v[152:153]
	v_mul_f32_e32 v0, v75, v75
	v_pk_fma_f32 v[72:73], v[72:73], v[174:175], v[222:223]
	v_pk_fma_f32 v[150:151], v[150:151], v[150:151], v[152:153]
	v_pk_fma_f32 v[152:153], v[74:75], v[74:75], v[0:1] op_sel_hi:[1,1,0]
	v_mul_f32_e32 v0, v73, v73
	v_pk_fma_f32 v[70:71], v[70:71], v[176:177], v[224:225]
	v_pk_fma_f32 v[68:69], v[68:69], v[178:179], v[226:227]
	v_pk_add_f32 v[148:149], v[148:149], v[148:149] op_sel:[0,1] op_sel_hi:[1,0]
	v_pk_add_f32 v[150:151], v[150:151], v[150:151] op_sel:[0,1] op_sel_hi:[1,0]
	v_pk_fma_f32 v[154:155], v[72:73], v[72:73], v[0:1] op_sel_hi:[1,1,0]
	v_pk_mul_f32 v[156:157], v[70:71], v[70:71]
	v_pk_mul_f32 v[158:159], v[68:69], v[68:69]
	v_mov_b32_e32 v149, v156
	v_mov_b32_e32 v151, v157
	v_mov_b32_e32 v153, v158
	v_mov_b32_e32 v155, v159
	v_pk_fma_f32 v[66:67], v[66:67], v[180:181], v[228:229]
	v_pk_fma_f32 v[64:65], v[64:65], v[182:183], v[230:231]
	v_pk_add_f32 v[148:149], v[148:149], v[150:151]
	v_pk_add_f32 v[150:151], v[152:153], v[154:155]
	v_mov_b32_e32 v152, v67
	v_mov_b32_e32 v153, v65
	v_pk_fma_f32 v[62:63], v[62:63], v[184:185], v[232:233]
	s_waitcnt vmcnt(5)
	v_lshlrev_b32_e32 v236, 16, v112
	v_and_b32_e32 v237, 0xffff0000, v112
	v_lshlrev_b32_e32 v238, 16, v113
	v_and_b32_e32 v239, 0xffff0000, v113
	v_pk_add_f32 v[148:149], v[148:149], v[150:151]
	v_mov_b32_e32 v150, v66
	v_mov_b32_e32 v151, v64
	v_pk_mul_f32 v[152:153], v[152:153], v[152:153]
	v_mul_f32_e32 v0, v63, v63
	v_pk_fma_f32 v[60:61], v[60:61], v[186:187], v[234:235]
	s_waitcnt vmcnt(4)
	v_lshlrev_b32_e32 v130, 16, v114
	v_and_b32_e32 v131, 0xffff0000, v114
	v_lshlrev_b32_e32 v128, 16, v115
	v_and_b32_e32 v129, 0xffff0000, v115
	v_pk_fma_f32 v[150:151], v[150:151], v[150:151], v[152:153]
	v_pk_fma_f32 v[152:153], v[62:63], v[62:63], v[0:1] op_sel_hi:[1,1,0]
	v_mul_f32_e32 v0, v61, v61
	v_pk_fma_f32 v[58:59], v[58:59], v[188:189], v[236:237]
	v_pk_fma_f32 v[56:57], v[56:57], v[190:191], v[238:239]
	s_waitcnt vmcnt(3)
	v_lshlrev_b32_e32 v126, 16, v116
	v_and_b32_e32 v127, 0xffff0000, v116
	v_pk_add_f32 v[148:149], v[148:149], v[148:149] op_sel:[0,1] op_sel_hi:[1,0]
	v_pk_add_f32 v[150:151], v[150:151], v[150:151] op_sel:[0,1] op_sel_hi:[1,0]
	v_pk_fma_f32 v[154:155], v[60:61], v[60:61], v[0:1] op_sel_hi:[1,1,0]
	v_pk_mul_f32 v[156:157], v[58:59], v[58:59]
	v_pk_mul_f32 v[158:159], v[56:57], v[56:57]
	v_pk_fma_f32 v[16:17], v[54:55], v[16:17], v[130:131]
	v_pk_fma_f32 v[18:19], v[52:53], v[18:19], v[128:129]
	v_lshlrev_b32_e32 v124, 16, v117
	v_and_b32_e32 v125, 0xffff0000, v117
	v_mov_b32_e32 v149, v156
	v_mov_b32_e32 v151, v157
	v_mov_b32_e32 v153, v158
	v_mov_b32_e32 v155, v159
	v_mov_b32_e32 v54, v17
	v_mov_b32_e32 v55, v19
	v_pk_fma_f32 v[12:13], v[50:51], v[12:13], v[126:127]
	v_pk_add_f32 v[148:149], v[148:149], v[150:151]
	v_pk_add_f32 v[150:151], v[152:153], v[154:155]
	v_mov_b32_e32 v52, v16
	v_mov_b32_e32 v53, v18
	v_pk_mul_f32 v[54:55], v[54:55], v[54:55]
	v_mul_f32_e32 v0, v13, v13
	v_pk_fma_f32 v[14:15], v[46:47], v[14:15], v[124:125]
	s_waitcnt vmcnt(2)
	v_lshlrev_b32_e32 v122, 16, v118
	v_and_b32_e32 v123, 0xffff0000, v118
	v_lshlrev_b32_e32 v120, 16, v119
	v_and_b32_e32 v121, 0xffff0000, v119
	s_waitcnt vmcnt(1)
	v_lshlrev_b32_e32 v118, 16, v192
	v_and_b32_e32 v119, 0xffff0000, v192
	v_pk_add_f32 v[148:149], v[148:149], v[150:151]
	v_pk_fma_f32 v[52:53], v[52:53], v[52:53], v[54:55]
	v_pk_fma_f32 v[50:51], v[12:13], v[12:13], v[0:1] op_sel_hi:[1,1,0]
	v_mul_f32_e32 v0, v15, v15
	v_lshlrev_b32_e32 v116, 16, v193
	v_and_b32_e32 v117, 0xffff0000, v193
	s_waitcnt vmcnt(0)
	v_lshlrev_b32_e32 v111, 16, v194
	v_pk_fma_f32 v[46:47], v[14:15], v[14:15], v[0:1] op_sel_hi:[1,1,0]
	v_pk_fma_f32 v[8:9], v[44:45], v[8:9], v[122:123]
	v_pk_fma_f32 v[4:5], v[40:41], v[4:5], v[118:119]
	v_pk_add_f32 v[44:45], v[148:149], v[148:149] op_sel:[0,1] op_sel_hi:[1,0]
	v_pk_add_f32 v[52:53], v[52:53], v[52:53] op_sel:[0,1] op_sel_hi:[1,0]
	v_mul_f32_e32 v0, v5, v5
	v_pk_fma_f32 v[6:7], v[38:39], v[6:7], v[116:117]
	v_mov_b32_e32 v45, v36
	v_mov_b32_e32 v53, v111
	v_mov_b32_e32 v51, v36
	v_mov_b32_e32 v47, v111
	v_pk_fma_f32 v[10:11], v[42:43], v[10:11], v[120:121]
	v_pk_fma_f32 v[40:41], v[4:5], v[4:5], v[0:1] op_sel_hi:[1,1,0]
	v_mul_f32_e32 v0, v7, v7
	v_pk_add_f32 v[54:55], v[44:45], v[52:53]
	v_pk_add_f32 v[44:45], v[50:51], v[46:47]
	v_and_b32_e32 v115, 0xffff0000, v194
	v_pk_mul_f32 v[42:43], v[10:11], v[10:11]
	v_pk_fma_f32 v[38:39], v[6:7], v[6:7], v[0:1] op_sel_hi:[1,1,0]
	v_pk_add_f32 v[46:47], v[54:55], v[44:45]
	v_pk_mul_f32 v[44:45], v[54:55], v[44:45]
	v_mov_b32_e32 v36, v8
	v_mov_b32_e32 v0, v8
	v_mul_f32_e32 v114, v9, v9
	v_lshlrev_b32_e32 v112, 16, v195
	v_and_b32_e32 v113, 0xffff0000, v195
	v_mov_b32_e32 v47, v45
	v_mov_b32_e32 v44, v10
	v_mov_b32_e32 v45, v37
	v_mov_b32_e32 v50, v10
	v_mov_b32_e32 v51, v1
	v_pk_fma_f32 v[0:1], v[36:37], v[0:1], v[114:115]
	v_mov_b32_e32 v114, v43
	v_pk_fma_f32 v[36:37], v[44:45], v[50:51], v[114:115]
	v_pk_fma_f32 v[2:3], v[34:35], v[2:3], v[112:113]
	v_pk_add_f32 v[42:43], v[0:1], v[36:37]
	v_pk_mul_f32 v[36:37], v[0:1], v[36:37]
	v_pk_mul_f32 v[34:35], v[2:3], v[2:3]
	v_mov_b32_e32 v43, v37
	v_mov_b32_e32 v41, v34
	v_mov_b32_e32 v39, v35
	v_pk_add_f32 v[36:37], v[46:47], v[42:43]
	v_pk_add_f32 v[34:35], v[40:41], v[38:39]
	v_add_u32_e32 v46, 0x700, v22
	v_pk_add_f32 v[34:35], v[36:37], v[34:35]
	v_lshl_add_u64 v[148:149], v[22:23], 2, s[10:11]
	v_add_f32_e32 v0, v34, v35
	ds_bpermute_b32 v34, v132, v0
	v_add_u32_e32 v54, 0x14100, v48
	v_lshl_add_u64 v[156:157], v[26:27], 2, s[10:11]
	v_lshl_add_u64 v[158:159], v[28:29], 2, s[10:11]
	v_lshl_add_u64 v[150:151], v[108:109], 2, s[10:11]
	s_waitcnt lgkmcnt(0)
	v_add_f32_e32 v0, v0, v34
	ds_bpermute_b32 v34, v133, v0
	v_lshl_add_u64 v[152:153], v[106:107], 2, s[10:11]
	v_lshl_add_u64 v[154:155], v[24:25], 2, s[10:11]
	v_ashrrev_i32_e32 v111, 31, v110
	v_lshl_add_u64 v[110:111], v[110:111], 2, s[10:11]
	s_waitcnt lgkmcnt(0)
	v_add_f32_e32 v0, v0, v34
	ds_bpermute_b32 v22, v134, v0
	ds_read_b128 v[34:37], v54
	ds_read_b128 v[38:41], v54 offset:1024
	ds_read_b128 v[42:45], v54 offset:2048
	ds_read_b128 v[50:53], v54 offset:3072
	ds_read_b128 v[112:115], v54 offset:4096
	ds_read_b128 v[116:119], v54 offset:5120
	ds_read_b128 v[106:109], v54 offset:6144
	ds_read_b128 v[120:123], v54 offset:7168
	v_ashrrev_i32_e32 v47, 31, v46
	s_waitcnt lgkmcnt(8)
	v_add_f32_e32 v0, v0, v22
	ds_bpermute_b32 v22, v135, v0
	v_lshl_add_u64 v[46:47], v[46:47], 2, s[10:11]
	s_waitcnt lgkmcnt(0)
	v_add_f32_e32 v0, v0, v22
	ds_bpermute_b32 v22, v136, v0
	s_waitcnt lgkmcnt(0)
	v_add_f32_e32 v0, v0, v22
	ds_bpermute_b32 v48, v137, v0
	ds_read_b128 v[22:25], v54 offset:8192
	ds_read_b128 v[124:127], v54 offset:9216
	ds_read_b128 v[128:131], v54 offset:10240
	s_waitcnt lgkmcnt(3)
	v_add_f32_e32 v0, v0, v48
	v_fmamk_f32 v0, v0, 0x39800000, v139
	v_mul_f32_e32 v26, 0x4f800000, v0
	v_cmp_gt_f32_e32 vcc, s47, v0
	s_nop 1
	v_cndmask_b32_e32 v0, v0, v26, vcc
	v_sqrt_f32_e32 v26, v0
	s_nop 0
	v_add_u32_e32 v27, -1, v26
	v_fma_f32 v28, -v27, v26, v0
	v_cmp_ge_f32_e64 s[0:1], 0, v28
	v_add_u32_e32 v28, 1, v26
	s_nop 0
	v_cndmask_b32_e64 v27, v26, v27, s[0:1]
	v_fma_f32 v26, -v28, v26, v0
	v_cmp_lt_f32_e64 s[0:1], 0, v26
	s_nop 1
	v_cndmask_b32_e64 v26, v27, v28, s[0:1]
	v_mul_f32_e32 v27, 0x37800000, v26
	v_cndmask_b32_e32 v26, v26, v27, vcc
	v_cmp_class_f32_e32 vcc, v0, v140
	s_nop 1
	v_cndmask_b32_e32 v26, v26, v0, vcc
	v_div_scale_f32 v27, s[0:1], v26, v26, 1.0
	v_rcp_f32_e32 v28, v27
	v_mov_b32_e32 v0, v55
	s_mov_b64 s[0:1], 0
	v_fma_f32 v29, -v27, v28, 1.0
	v_fmac_f32_e32 v28, v29, v28
	v_div_scale_f32 v29, vcc, 1.0, v26, 1.0
	v_mul_f32_e32 v48, v29, v28
	v_fma_f32 v55, -v27, v48, v29
	v_fmac_f32_e32 v48, v55, v28
	v_fma_f32 v27, -v27, v48, v29
	v_div_fmas_f32 v27, v27, v28, v48
	v_div_fixup_f32 v48, v27, v26, 1.0
	v_pk_mul_f32 v[26:27], v[96:97], v[48:49] op_sel_hi:[1,0]
	v_pk_mul_f32 v[28:29], v[98:99], v[48:49] op_sel_hi:[1,0]
	v_pk_mul_f32 v[26:27], v[34:35], v[26:27]
	v_pk_mul_f32 v[28:29], v[36:37], v[28:29]
	global_store_dwordx4 v[148:149], v[26:29], off
	v_pk_mul_f32 v[16:17], v[16:17], v[48:49] op_sel_hi:[1,0]
	v_pk_mul_f32 v[18:19], v[18:19], v[48:49] op_sel_hi:[1,0]
	v_pk_mul_f32 v[26:27], v[94:95], v[48:49] op_sel_hi:[1,0]
	v_pk_mul_f32 v[28:29], v[92:93], v[48:49] op_sel_hi:[1,0]
	v_pk_mul_f32 v[26:27], v[38:39], v[26:27]
	v_pk_mul_f32 v[28:29], v[40:41], v[28:29]
	global_store_dwordx4 v[148:149], v[26:29], off offset:1024
	v_pk_mul_f32 v[8:9], v[8:9], v[48:49] op_sel_hi:[1,0]
	v_pk_mul_f32 v[10:11], v[10:11], v[48:49] op_sel_hi:[1,0]
	v_pk_mul_f32 v[26:27], v[90:91], v[48:49] op_sel_hi:[1,0]
	v_pk_mul_f32 v[28:29], v[88:89], v[48:49] op_sel_hi:[1,0]
	v_pk_mul_f32 v[26:27], v[42:43], v[26:27]
	v_pk_mul_f32 v[28:29], v[44:45], v[28:29]
	global_store_dwordx4 v[148:149], v[26:29], off offset:2048
	v_pk_mul_f32 v[0:1], v[0:1], v[48:49] op_sel_hi:[1,0]
	v_pk_mul_f32 v[2:3], v[2:3], v[48:49] op_sel_hi:[1,0]
	v_pk_mul_f32 v[26:27], v[86:87], v[48:49] op_sel_hi:[1,0]
	v_pk_mul_f32 v[28:29], v[84:85], v[48:49] op_sel_hi:[1,0]
	v_pk_mul_f32 v[26:27], v[50:51], v[26:27]
	v_pk_mul_f32 v[28:29], v[52:53], v[28:29]
	global_store_dwordx4 v[148:149], v[26:29], off offset:3072
	s_and_b64 vcc, exec, s[2:3]
	s_nop 0
	v_pk_mul_f32 v[26:27], v[82:83], v[48:49] op_sel_hi:[1,0]
	v_pk_mul_f32 v[28:29], v[80:81], v[48:49] op_sel_hi:[1,0]
	v_pk_mul_f32 v[26:27], v[112:113], v[26:27]
	v_pk_mul_f32 v[28:29], v[114:115], v[28:29]
	global_store_dwordx4 v[150:151], v[26:29], off
	s_nop 1
	v_pk_mul_f32 v[26:27], v[78:79], v[48:49] op_sel_hi:[1,0]
	v_pk_mul_f32 v[28:29], v[76:77], v[48:49] op_sel_hi:[1,0]
	v_pk_mul_f32 v[26:27], v[116:117], v[26:27]
	v_pk_mul_f32 v[28:29], v[118:119], v[28:29]
	global_store_dwordx4 v[152:153], v[26:29], off
	s_nop 1
	v_pk_mul_f32 v[26:27], v[74:75], v[48:49] op_sel_hi:[1,0]
	v_pk_mul_f32 v[28:29], v[72:73], v[48:49] op_sel_hi:[1,0]
	v_pk_mul_f32 v[26:27], v[26:27], v[106:107]
	v_pk_mul_f32 v[28:29], v[28:29], v[108:109]
	global_store_dwordx4 v[110:111], v[26:29], off
	s_nop 1
	v_pk_mul_f32 v[26:27], v[70:71], v[48:49] op_sel_hi:[1,0]
	v_pk_mul_f32 v[28:29], v[68:69], v[48:49] op_sel_hi:[1,0]
	v_pk_mul_f32 v[26:27], v[26:27], v[120:121]
	v_pk_mul_f32 v[28:29], v[28:29], v[122:123]
	global_store_dwordx4 v[46:47], v[26:29], off
	s_nop 1
	v_pk_mul_f32 v[26:27], v[66:67], v[48:49] op_sel_hi:[1,0]
	v_pk_mul_f32 v[28:29], v[64:65], v[48:49] op_sel_hi:[1,0]
	s_waitcnt lgkmcnt(2)
	v_pk_mul_f32 v[22:23], v[26:27], v[22:23]
	v_pk_mul_f32 v[24:25], v[28:29], v[24:25]
	global_store_dwordx4 v[154:155], v[22:25], off
	v_pk_mul_f32 v[26:27], v[58:59], v[48:49] op_sel_hi:[1,0]
	v_pk_mul_f32 v[28:29], v[56:57], v[48:49] op_sel_hi:[1,0]
	v_pk_mul_f32 v[22:23], v[62:63], v[48:49] op_sel_hi:[1,0]
	v_pk_mul_f32 v[24:25], v[60:61], v[48:49] op_sel_hi:[1,0]
	s_waitcnt lgkmcnt(1)
	v_pk_mul_f32 v[22:23], v[22:23], v[124:125]
	v_pk_mul_f32 v[24:25], v[24:25], v[126:127]
	global_store_dwordx4 v[156:157], v[22:25], off
	ds_read_b128 v[22:25], v54 offset:11264
	s_waitcnt lgkmcnt(1)
	v_pk_mul_f32 v[28:29], v[28:29], v[130:131]
	v_pk_mul_f32 v[26:27], v[26:27], v[128:129]
	global_store_dwordx4 v[158:159], v[26:29], off
	s_waitcnt lgkmcnt(0)
	v_pk_mul_f32 v[18:19], v[18:19], v[24:25]
	v_pk_mul_f32 v[16:17], v[16:17], v[22:23]
	ds_read_b128 v[22:25], v54 offset:12288
	global_store_dwordx4 v[30:31], v[16:19], off
	s_nop 1
	v_pk_mul_f32 v[16:17], v[12:13], v[48:49] op_sel_hi:[1,0]
	v_pk_mul_f32 v[18:19], v[14:15], v[48:49] op_sel_hi:[1,0]
	ds_read_b128 v[12:15], v54 offset:13312
	s_waitcnt lgkmcnt(1)
	v_pk_mul_f32 v[18:19], v[18:19], v[24:25]
	v_pk_mul_f32 v[16:17], v[16:17], v[22:23]
	global_store_dwordx4 v[102:103], v[16:19], off
	s_waitcnt lgkmcnt(0)
	v_pk_mul_f32 v[10:11], v[10:11], v[14:15]
	v_pk_mul_f32 v[8:9], v[8:9], v[12:13]
	ds_read_b128 v[12:15], v54 offset:14336
	global_store_dwordx4 v[100:101], v[8:11], off
	s_nop 1
	v_pk_mul_f32 v[10:11], v[6:7], v[48:49] op_sel_hi:[1,0]
	v_pk_mul_f32 v[8:9], v[4:5], v[48:49] op_sel_hi:[1,0]
	ds_read_b128 v[4:7], v54 offset:15360
	s_waitcnt lgkmcnt(1)
	v_pk_mul_f32 v[8:9], v[8:9], v[12:13]
	v_pk_mul_f32 v[10:11], v[10:11], v[14:15]
	global_store_dwordx4 v[104:105], v[8:11], off
	s_waitcnt lgkmcnt(0)
	v_pk_mul_f32 v[0:1], v[0:1], v[4:5]
	v_pk_mul_f32 v[2:3], v[2:3], v[6:7]
	v_lshl_add_u64 v[4:5], v[20:21], 2, s[10:11]
	global_store_dwordx4 v[4:5], v[0:3], off
	s_cbranch_vccz .LBB0_1584
	s_add_i32 s77, s77, s97
	s_cmpk_gt_i32 s77, 0x1ff
	s_barrier
	s_cbranch_scc0 .LBB0_1498
